# chain consumer loop rescheduled (LDS reads ahead, deferred Y store); adaLN GEMV 48 loads in flight with v_fmac; SwiGLU epilogue clamp via min/med3 on raw accumulators (no canonicalize)
# speedup vs baseline: 1.0122x; 1.0122x over previous
; DI void phase_prologue(const Frame& F) {
;     ...
;     for (int u = F.vcu; u < 4 * 96; u += F.G) {
;         const int l = u / 96, nb = u % 96, kq = F.wave, n = nb * 64 + F.lane;
;         float acc[8];
; #pragma unroll
;         for (int b = 0; b < 8; ++b) acc[b] = 0.f;
;         const float* wp = F.ap->in[2] + ((size_t)l * D + kq * 128) * 6144 + n;
; #pragma unroll 4
;         for (int k = 0; k < 128; ++k) { const float wv = wp[(size_t)k * 6144];
; #pragma unroll
;             for (int b = 0; b < 8; ++b) acc[b] += ca[b * D + kq * 128 + k] * wv; }
.LBB0_51:
	s_mul_hi_i32 s4, s3, 0x2aaaaaab
	s_lshr_b32 s5, s4, 31
	s_ashr_i32 s4, s4, 4
	s_add_i32 s4, s4, s5
	s_mul_i32 s5, s4, 0x60
	s_sub_i32 s5, s3, s5
	v_lshl_or_b32 v0, s5, 6, v14
	s_ashr_i32 s5, s4, 31
	s_lshl_b64 s[14:15], s[4:5], 10
	s_add_u32 s13, s14, s7
	s_addc_u32 s14, s15, s8
	s_mulk_i32 s14, 0x6000
	s_mul_hi_u32 s15, s13, 0x6000
	s_add_i32 s15, s15, s14
	s_mulk_i32 s13, 0x6000
	s_waitcnt lgkmcnt(0)
	s_add_u32 s14, s36, s13
	s_addc_u32 s15, s37, s15
	v_ashrrev_i32_e32 v1, 31, v0
	v_mov_b32_e32 v4, 0
	v_lshl_add_u64 v[2:3], v[0:1], 2, s[14:15]
	s_mov_b64 s[20:21], 0
	s_mov_b32 s13, s9
	v_mov_b32_e32 v5, v4
	v_mov_b32_e32 v6, v4
	v_mov_b32_e32 v7, v4
	v_mov_b32_e32 v8, v4
	v_mov_b32_e32 v9, v4
	v_mov_b32_e32 v10, v4
	v_mov_b32_e32 v11, v4
	v_lshlrev_b32_e32 v48, 2, v0
	v_mov_b32_e32 v15, s9
	global_load_dword v64, v48, s[14:15]
	s_add_u32 s14, s14, 0x6000
	s_addc_u32 s15, s15, 0
	global_load_dword v65, v48, s[14:15]
	s_add_u32 s14, s14, 0x6000
	s_addc_u32 s15, s15, 0
	global_load_dword v66, v48, s[14:15]
	s_add_u32 s14, s14, 0x6000
	s_addc_u32 s15, s15, 0
	global_load_dword v67, v48, s[14:15]
	s_add_u32 s14, s14, 0x6000
	s_addc_u32 s15, s15, 0
	global_load_dword v68, v48, s[14:15]
	s_add_u32 s14, s14, 0x6000
	s_addc_u32 s15, s15, 0
	global_load_dword v69, v48, s[14:15]
	s_add_u32 s14, s14, 0x6000
	s_addc_u32 s15, s15, 0
	global_load_dword v70, v48, s[14:15]
	s_add_u32 s14, s14, 0x6000
	s_addc_u32 s15, s15, 0
	global_load_dword v71, v48, s[14:15]
	s_add_u32 s14, s14, 0x6000
	s_addc_u32 s15, s15, 0
	global_load_dword v72, v48, s[14:15]
	s_add_u32 s14, s14, 0x6000
	s_addc_u32 s15, s15, 0
	global_load_dword v73, v48, s[14:15]
	s_add_u32 s14, s14, 0x6000
	s_addc_u32 s15, s15, 0
	global_load_dword v74, v48, s[14:15]
	s_add_u32 s14, s14, 0x6000
	s_addc_u32 s15, s15, 0
	global_load_dword v75, v48, s[14:15]
	s_add_u32 s14, s14, 0x6000
	s_addc_u32 s15, s15, 0
	global_load_dword v76, v48, s[14:15]
	s_add_u32 s14, s14, 0x6000
	s_addc_u32 s15, s15, 0
	global_load_dword v77, v48, s[14:15]
	s_add_u32 s14, s14, 0x6000
	s_addc_u32 s15, s15, 0
	global_load_dword v78, v48, s[14:15]
	s_add_u32 s14, s14, 0x6000
	s_addc_u32 s15, s15, 0
	global_load_dword v79, v48, s[14:15]
	s_add_u32 s14, s14, 0x6000
	s_addc_u32 s15, s15, 0
	global_load_dword v112, v48, s[14:15]
	s_add_u32 s14, s14, 0x6000
	s_addc_u32 s15, s15, 0
	global_load_dword v113, v48, s[14:15]
	s_add_u32 s14, s14, 0x6000
	s_addc_u32 s15, s15, 0
	global_load_dword v114, v48, s[14:15]
	s_add_u32 s14, s14, 0x6000
	s_addc_u32 s15, s15, 0
	global_load_dword v115, v48, s[14:15]
	s_add_u32 s14, s14, 0x6000
	s_addc_u32 s15, s15, 0
	global_load_dword v116, v48, s[14:15]
	s_add_u32 s14, s14, 0x6000
	s_addc_u32 s15, s15, 0
	global_load_dword v117, v48, s[14:15]
	s_add_u32 s14, s14, 0x6000
	s_addc_u32 s15, s15, 0
	global_load_dword v118, v48, s[14:15]
	s_add_u32 s14, s14, 0x6000
	s_addc_u32 s15, s15, 0
	global_load_dword v119, v48, s[14:15]
	s_add_u32 s14, s14, 0x6000
	s_addc_u32 s15, s15, 0
	global_load_dword v120, v48, s[14:15]
	s_add_u32 s14, s14, 0x6000
	s_addc_u32 s15, s15, 0
	global_load_dword v121, v48, s[14:15]
	s_add_u32 s14, s14, 0x6000
	s_addc_u32 s15, s15, 0
	global_load_dword v122, v48, s[14:15]
	s_add_u32 s14, s14, 0x6000
	s_addc_u32 s15, s15, 0
	global_load_dword v123, v48, s[14:15]
	s_add_u32 s14, s14, 0x6000
	s_addc_u32 s15, s15, 0
	global_load_dword v124, v48, s[14:15]
	s_add_u32 s14, s14, 0x6000
	s_addc_u32 s15, s15, 0
	global_load_dword v125, v48, s[14:15]
	s_add_u32 s14, s14, 0x6000
	s_addc_u32 s15, s15, 0
	global_load_dword v126, v48, s[14:15]
	s_add_u32 s14, s14, 0x6000
	s_addc_u32 s15, s15, 0
	global_load_dword v127, v48, s[14:15]
	s_add_u32 s14, s14, 0x6000
	s_addc_u32 s15, s15, 0
	global_load_dword v149, v48, s[14:15]
	s_add_u32 s14, s14, 0x6000
	s_addc_u32 s15, s15, 0
	global_load_dword v150, v48, s[14:15]
	s_add_u32 s14, s14, 0x6000
	s_addc_u32 s15, s15, 0
	global_load_dword v151, v48, s[14:15]
	s_add_u32 s14, s14, 0x6000
	s_addc_u32 s15, s15, 0
	global_load_dword v152, v48, s[14:15]
	s_add_u32 s14, s14, 0x6000
	s_addc_u32 s15, s15, 0
	global_load_dword v153, v48, s[14:15]
	s_add_u32 s14, s14, 0x6000
	s_addc_u32 s15, s15, 0
	global_load_dword v154, v48, s[14:15]
	s_add_u32 s14, s14, 0x6000
	s_addc_u32 s15, s15, 0
	global_load_dword v155, v48, s[14:15]
	s_add_u32 s14, s14, 0x6000
	s_addc_u32 s15, s15, 0
	global_load_dword v156, v48, s[14:15]
	s_add_u32 s14, s14, 0x6000
	s_addc_u32 s15, s15, 0
	global_load_dword v157, v48, s[14:15]
	s_add_u32 s14, s14, 0x6000
	s_addc_u32 s15, s15, 0
	global_load_dword v158, v48, s[14:15]
	s_add_u32 s14, s14, 0x6000
	s_addc_u32 s15, s15, 0
	global_load_dword v159, v48, s[14:15]
	s_add_u32 s14, s14, 0x6000
	s_addc_u32 s15, s15, 0
	global_load_dword v160, v48, s[14:15]
	s_add_u32 s14, s14, 0x6000
	s_addc_u32 s15, s15, 0
	global_load_dword v161, v48, s[14:15]
	s_add_u32 s14, s14, 0x6000
	s_addc_u32 s15, s15, 0
	global_load_dword v162, v48, s[14:15]
	s_add_u32 s14, s14, 0x6000
	s_addc_u32 s15, s15, 0
	global_load_dword v163, v48, s[14:15]
	s_add_u32 s14, s14, 0x6000
	s_addc_u32 s15, s15, 0
	global_load_dword v164, v48, s[14:15]
	s_add_u32 s14, s14, 0x6000
	s_addc_u32 s15, s15, 0
	global_load_dword v165, v48, s[14:15]
	s_add_u32 s14, s14, 0x6000
	s_addc_u32 s15, s15, 0
	global_load_dword v166, v48, s[14:15]
	s_add_u32 s14, s14, 0x6000
	s_addc_u32 s15, s15, 0
	global_load_dword v167, v48, s[14:15]
	s_add_u32 s14, s14, 0x6000
	s_addc_u32 s15, s15, 0
	global_load_dword v168, v48, s[14:15]
	s_add_u32 s14, s14, 0x6000
	s_addc_u32 s15, s15, 0
	global_load_dword v169, v48, s[14:15]
	s_add_u32 s14, s14, 0x6000
	s_addc_u32 s15, s15, 0
	global_load_dword v170, v48, s[14:15]
	s_add_u32 s14, s14, 0x6000
	s_addc_u32 s15, s15, 0
	global_load_dword v171, v48, s[14:15]
	s_add_u32 s14, s14, 0x6000
	s_addc_u32 s15, s15, 0
	global_load_dword v172, v48, s[14:15]
	s_add_u32 s14, s14, 0x6000
	s_addc_u32 s15, s15, 0
	global_load_dword v173, v48, s[14:15]
	s_add_u32 s14, s14, 0x6000
	s_addc_u32 s15, s15, 0
	global_load_dword v174, v48, s[14:15]
	s_add_u32 s14, s14, 0x6000
	s_addc_u32 s15, s15, 0
	global_load_dword v175, v48, s[14:15]
	s_add_u32 s14, s14, 0x6000
	s_addc_u32 s15, s15, 0
	global_load_dword v176, v48, s[14:15]
	s_add_u32 s14, s14, 0x6000
	s_addc_u32 s15, s15, 0
	global_load_dword v177, v48, s[14:15]
	s_add_u32 s14, s14, 0x6000
	s_addc_u32 s15, s15, 0
	global_load_dword v178, v48, s[14:15]
	s_add_u32 s14, s14, 0x6000
	s_addc_u32 s15, s15, 0
	global_load_dword v179, v48, s[14:15]
	s_add_u32 s14, s14, 0x6000
	s_addc_u32 s15, s15, 0
	global_load_dword v180, v48, s[14:15]
	s_add_u32 s14, s14, 0x6000
	s_addc_u32 s15, s15, 0
	s_waitcnt vmcnt(48)
; DI void phase_prologue(const Frame& F) {
;     ...
;         for (int k = 0; k < 128; ++k) { const float wv = wp[(size_t)k * 6144];
; #pragma unroll
;             for (int b = 0; b < 8; ++b) acc[b] += ca[b * D + kq * 128 + k] * wv; }
	ds_read_b128 v[16:19], v15 offset:0
	ds_read_b128 v[20:23], v15 offset:4096
	ds_read_b128 v[24:27], v15 offset:8192
	ds_read_b128 v[28:31], v15 offset:12288
	ds_read_b128 v[32:35], v15 offset:16384
	ds_read_b128 v[36:39], v15 offset:20480
	ds_read_b128 v[40:43], v15 offset:24576
	ds_read_b128 v[44:47], v15 offset:28672
	s_waitcnt lgkmcnt(7)
	v_fmac_f32_e32 v6, v64, v16
	v_fmac_f32_e32 v6, v65, v17
	v_fmac_f32_e32 v6, v66, v18
	v_fmac_f32_e32 v6, v67, v19
	s_waitcnt lgkmcnt(6)
	v_fmac_f32_e32 v7, v64, v20
	v_fmac_f32_e32 v7, v65, v21
	v_fmac_f32_e32 v7, v66, v22
	v_fmac_f32_e32 v7, v67, v23
	s_waitcnt lgkmcnt(5)
	v_fmac_f32_e32 v8, v64, v24
	v_fmac_f32_e32 v8, v65, v25
	v_fmac_f32_e32 v8, v66, v26
	v_fmac_f32_e32 v8, v67, v27
	s_waitcnt lgkmcnt(4)
	v_fmac_f32_e32 v9, v64, v28
	v_fmac_f32_e32 v9, v65, v29
	v_fmac_f32_e32 v9, v66, v30
	v_fmac_f32_e32 v9, v67, v31
	s_waitcnt lgkmcnt(3)
	v_fmac_f32_e32 v10, v64, v32
	v_fmac_f32_e32 v10, v65, v33
	v_fmac_f32_e32 v10, v66, v34
	v_fmac_f32_e32 v10, v67, v35
	s_waitcnt lgkmcnt(2)
	v_fmac_f32_e32 v11, v64, v36
	v_fmac_f32_e32 v11, v65, v37
	v_fmac_f32_e32 v11, v66, v38
	v_fmac_f32_e32 v11, v67, v39
	s_waitcnt lgkmcnt(1)
	v_fmac_f32_e32 v4, v64, v40
	v_fmac_f32_e32 v4, v65, v41
	v_fmac_f32_e32 v4, v66, v42
	v_fmac_f32_e32 v4, v67, v43
	s_waitcnt lgkmcnt(0)
	v_fmac_f32_e32 v5, v64, v44
	v_fmac_f32_e32 v5, v65, v45
	v_fmac_f32_e32 v5, v66, v46
	v_fmac_f32_e32 v5, v67, v47
	ds_read_b128 v[16:19], v15 offset:16
	ds_read_b128 v[20:23], v15 offset:4112
	ds_read_b128 v[24:27], v15 offset:8208
	ds_read_b128 v[28:31], v15 offset:12304
	ds_read_b128 v[32:35], v15 offset:16400
	ds_read_b128 v[36:39], v15 offset:20496
	ds_read_b128 v[40:43], v15 offset:24592
	ds_read_b128 v[44:47], v15 offset:28688
	s_waitcnt lgkmcnt(7)
	v_fmac_f32_e32 v6, v68, v16
	v_fmac_f32_e32 v6, v69, v17
	v_fmac_f32_e32 v6, v70, v18
	v_fmac_f32_e32 v6, v71, v19
	s_waitcnt lgkmcnt(6)
	v_fmac_f32_e32 v7, v68, v20
	v_fmac_f32_e32 v7, v69, v21
	v_fmac_f32_e32 v7, v70, v22
	v_fmac_f32_e32 v7, v71, v23
	s_waitcnt lgkmcnt(5)
	v_fmac_f32_e32 v8, v68, v24
	v_fmac_f32_e32 v8, v69, v25
	v_fmac_f32_e32 v8, v70, v26
	v_fmac_f32_e32 v8, v71, v27
	s_waitcnt lgkmcnt(4)
	v_fmac_f32_e32 v9, v68, v28
	v_fmac_f32_e32 v9, v69, v29
	v_fmac_f32_e32 v9, v70, v30
	v_fmac_f32_e32 v9, v71, v31
	s_waitcnt lgkmcnt(3)
	v_fmac_f32_e32 v10, v68, v32
	v_fmac_f32_e32 v10, v69, v33
	v_fmac_f32_e32 v10, v70, v34
	v_fmac_f32_e32 v10, v71, v35
	s_waitcnt lgkmcnt(2)
	v_fmac_f32_e32 v11, v68, v36
	v_fmac_f32_e32 v11, v69, v37
	v_fmac_f32_e32 v11, v70, v38
	v_fmac_f32_e32 v11, v71, v39
	s_waitcnt lgkmcnt(1)
	v_fmac_f32_e32 v4, v68, v40
	v_fmac_f32_e32 v4, v69, v41
	v_fmac_f32_e32 v4, v70, v42
	v_fmac_f32_e32 v4, v71, v43
	s_waitcnt lgkmcnt(0)
	v_fmac_f32_e32 v5, v68, v44
	v_fmac_f32_e32 v5, v69, v45
	v_fmac_f32_e32 v5, v70, v46
	v_fmac_f32_e32 v5, v71, v47
	ds_read_b128 v[16:19], v15 offset:32
	ds_read_b128 v[20:23], v15 offset:4128
	ds_read_b128 v[24:27], v15 offset:8224
	ds_read_b128 v[28:31], v15 offset:12320
	ds_read_b128 v[32:35], v15 offset:16416
	ds_read_b128 v[36:39], v15 offset:20512
	ds_read_b128 v[40:43], v15 offset:24608
	ds_read_b128 v[44:47], v15 offset:28704
	s_waitcnt lgkmcnt(7)
	v_fmac_f32_e32 v6, v72, v16
	v_fmac_f32_e32 v6, v73, v17
	v_fmac_f32_e32 v6, v74, v18
	v_fmac_f32_e32 v6, v75, v19
	s_waitcnt lgkmcnt(6)
	v_fmac_f32_e32 v7, v72, v20
	v_fmac_f32_e32 v7, v73, v21
	v_fmac_f32_e32 v7, v74, v22
	v_fmac_f32_e32 v7, v75, v23
	s_waitcnt lgkmcnt(5)
	v_fmac_f32_e32 v8, v72, v24
	v_fmac_f32_e32 v8, v73, v25
	v_fmac_f32_e32 v8, v74, v26
	v_fmac_f32_e32 v8, v75, v27
	s_waitcnt lgkmcnt(4)
	v_fmac_f32_e32 v9, v72, v28
	v_fmac_f32_e32 v9, v73, v29
	v_fmac_f32_e32 v9, v74, v30
	v_fmac_f32_e32 v9, v75, v31
	s_waitcnt lgkmcnt(3)
	v_fmac_f32_e32 v10, v72, v32
	v_fmac_f32_e32 v10, v73, v33
	v_fmac_f32_e32 v10, v74, v34
	v_fmac_f32_e32 v10, v75, v35
	s_waitcnt lgkmcnt(2)
	v_fmac_f32_e32 v11, v72, v36
	v_fmac_f32_e32 v11, v73, v37
	v_fmac_f32_e32 v11, v74, v38
	v_fmac_f32_e32 v11, v75, v39
	s_waitcnt lgkmcnt(1)
	v_fmac_f32_e32 v4, v72, v40
	v_fmac_f32_e32 v4, v73, v41
	v_fmac_f32_e32 v4, v74, v42
	v_fmac_f32_e32 v4, v75, v43
	s_waitcnt lgkmcnt(0)
	v_fmac_f32_e32 v5, v72, v44
	v_fmac_f32_e32 v5, v73, v45
	v_fmac_f32_e32 v5, v74, v46
	v_fmac_f32_e32 v5, v75, v47
	ds_read_b128 v[16:19], v15 offset:48
	ds_read_b128 v[20:23], v15 offset:4144
	ds_read_b128 v[24:27], v15 offset:8240
	ds_read_b128 v[28:31], v15 offset:12336
	ds_read_b128 v[32:35], v15 offset:16432
	ds_read_b128 v[36:39], v15 offset:20528
	ds_read_b128 v[40:43], v15 offset:24624
	ds_read_b128 v[44:47], v15 offset:28720
	s_waitcnt lgkmcnt(7)
	v_fmac_f32_e32 v6, v76, v16
	v_fmac_f32_e32 v6, v77, v17
	v_fmac_f32_e32 v6, v78, v18
	v_fmac_f32_e32 v6, v79, v19
	s_waitcnt lgkmcnt(6)
	v_fmac_f32_e32 v7, v76, v20
	v_fmac_f32_e32 v7, v77, v21
	v_fmac_f32_e32 v7, v78, v22
	v_fmac_f32_e32 v7, v79, v23
	s_waitcnt lgkmcnt(5)
	v_fmac_f32_e32 v8, v76, v24
	v_fmac_f32_e32 v8, v77, v25
	v_fmac_f32_e32 v8, v78, v26
	v_fmac_f32_e32 v8, v79, v27
	s_waitcnt lgkmcnt(4)
	v_fmac_f32_e32 v9, v76, v28
	v_fmac_f32_e32 v9, v77, v29
	v_fmac_f32_e32 v9, v78, v30
	v_fmac_f32_e32 v9, v79, v31
	s_waitcnt lgkmcnt(3)
	v_fmac_f32_e32 v10, v76, v32
	v_fmac_f32_e32 v10, v77, v33
	v_fmac_f32_e32 v10, v78, v34
	v_fmac_f32_e32 v10, v79, v35
	s_waitcnt lgkmcnt(2)
	v_fmac_f32_e32 v11, v76, v36
	v_fmac_f32_e32 v11, v77, v37
	v_fmac_f32_e32 v11, v78, v38
	v_fmac_f32_e32 v11, v79, v39
	s_waitcnt lgkmcnt(1)
	v_fmac_f32_e32 v4, v76, v40
	v_fmac_f32_e32 v4, v77, v41
	v_fmac_f32_e32 v4, v78, v42
	v_fmac_f32_e32 v4, v79, v43
	s_waitcnt lgkmcnt(0)
; DI void phase_prologue(const Frame& F) {
;     ...
;         for (int k = 0; k < 128; ++k) { const float wv = wp[(size_t)k * 6144];
; #pragma unroll
;             for (int b = 0; b < 8; ++b) acc[b] += ca[b * D + kq * 128 + k] * wv; }
	v_fmac_f32_e32 v5, v76, v44
	v_fmac_f32_e32 v5, v77, v45
	v_fmac_f32_e32 v5, v78, v46
	v_fmac_f32_e32 v5, v79, v47
	global_load_dword v64, v48, s[14:15]
	s_add_u32 s14, s14, 0x6000
	s_addc_u32 s15, s15, 0
	global_load_dword v65, v48, s[14:15]
	s_add_u32 s14, s14, 0x6000
	s_addc_u32 s15, s15, 0
	global_load_dword v66, v48, s[14:15]
	s_add_u32 s14, s14, 0x6000
	s_addc_u32 s15, s15, 0
	global_load_dword v67, v48, s[14:15]
	s_add_u32 s14, s14, 0x6000
	s_addc_u32 s15, s15, 0
	global_load_dword v68, v48, s[14:15]
	s_add_u32 s14, s14, 0x6000
	s_addc_u32 s15, s15, 0
	global_load_dword v69, v48, s[14:15]
	s_add_u32 s14, s14, 0x6000
	s_addc_u32 s15, s15, 0
	global_load_dword v70, v48, s[14:15]
	s_add_u32 s14, s14, 0x6000
	s_addc_u32 s15, s15, 0
	global_load_dword v71, v48, s[14:15]
	s_add_u32 s14, s14, 0x6000
	s_addc_u32 s15, s15, 0
	global_load_dword v72, v48, s[14:15]
	s_add_u32 s14, s14, 0x6000
	s_addc_u32 s15, s15, 0
	global_load_dword v73, v48, s[14:15]
	s_add_u32 s14, s14, 0x6000
	s_addc_u32 s15, s15, 0
	global_load_dword v74, v48, s[14:15]
	s_add_u32 s14, s14, 0x6000
	s_addc_u32 s15, s15, 0
	global_load_dword v75, v48, s[14:15]
	s_add_u32 s14, s14, 0x6000
	s_addc_u32 s15, s15, 0
	global_load_dword v76, v48, s[14:15]
	s_add_u32 s14, s14, 0x6000
	s_addc_u32 s15, s15, 0
	global_load_dword v77, v48, s[14:15]
	s_add_u32 s14, s14, 0x6000
	s_addc_u32 s15, s15, 0
	global_load_dword v78, v48, s[14:15]
	s_add_u32 s14, s14, 0x6000
	s_addc_u32 s15, s15, 0
	global_load_dword v79, v48, s[14:15]
	s_add_u32 s14, s14, 0x6000
	s_addc_u32 s15, s15, 0
	s_waitcnt vmcnt(48)
	ds_read_b128 v[16:19], v15 offset:64
	ds_read_b128 v[20:23], v15 offset:4160
	ds_read_b128 v[24:27], v15 offset:8256
	ds_read_b128 v[28:31], v15 offset:12352
	ds_read_b128 v[32:35], v15 offset:16448
	ds_read_b128 v[36:39], v15 offset:20544
	ds_read_b128 v[40:43], v15 offset:24640
	ds_read_b128 v[44:47], v15 offset:28736
	s_waitcnt lgkmcnt(7)
	v_fmac_f32_e32 v6, v112, v16
	v_fmac_f32_e32 v6, v113, v17
	v_fmac_f32_e32 v6, v114, v18
	v_fmac_f32_e32 v6, v115, v19
	s_waitcnt lgkmcnt(6)
	v_fmac_f32_e32 v7, v112, v20
	v_fmac_f32_e32 v7, v113, v21
	v_fmac_f32_e32 v7, v114, v22
	v_fmac_f32_e32 v7, v115, v23
	s_waitcnt lgkmcnt(5)
	v_fmac_f32_e32 v8, v112, v24
	v_fmac_f32_e32 v8, v113, v25
	v_fmac_f32_e32 v8, v114, v26
	v_fmac_f32_e32 v8, v115, v27
	s_waitcnt lgkmcnt(4)
	v_fmac_f32_e32 v9, v112, v28
	v_fmac_f32_e32 v9, v113, v29
	v_fmac_f32_e32 v9, v114, v30
	v_fmac_f32_e32 v9, v115, v31
	s_waitcnt lgkmcnt(3)
	v_fmac_f32_e32 v10, v112, v32
	v_fmac_f32_e32 v10, v113, v33
	v_fmac_f32_e32 v10, v114, v34
	v_fmac_f32_e32 v10, v115, v35
	s_waitcnt lgkmcnt(2)
	v_fmac_f32_e32 v11, v112, v36
	v_fmac_f32_e32 v11, v113, v37
	v_fmac_f32_e32 v11, v114, v38
	v_fmac_f32_e32 v11, v115, v39
	s_waitcnt lgkmcnt(1)
	v_fmac_f32_e32 v4, v112, v40
	v_fmac_f32_e32 v4, v113, v41
	v_fmac_f32_e32 v4, v114, v42
	v_fmac_f32_e32 v4, v115, v43
	s_waitcnt lgkmcnt(0)
	v_fmac_f32_e32 v5, v112, v44
	v_fmac_f32_e32 v5, v113, v45
	v_fmac_f32_e32 v5, v114, v46
	v_fmac_f32_e32 v5, v115, v47
	ds_read_b128 v[16:19], v15 offset:80
	ds_read_b128 v[20:23], v15 offset:4176
	ds_read_b128 v[24:27], v15 offset:8272
	ds_read_b128 v[28:31], v15 offset:12368
	ds_read_b128 v[32:35], v15 offset:16464
	ds_read_b128 v[36:39], v15 offset:20560
	ds_read_b128 v[40:43], v15 offset:24656
	ds_read_b128 v[44:47], v15 offset:28752
	s_waitcnt lgkmcnt(7)
	v_fmac_f32_e32 v6, v116, v16
	v_fmac_f32_e32 v6, v117, v17
	v_fmac_f32_e32 v6, v118, v18
	v_fmac_f32_e32 v6, v119, v19
	s_waitcnt lgkmcnt(6)
	v_fmac_f32_e32 v7, v116, v20
	v_fmac_f32_e32 v7, v117, v21
	v_fmac_f32_e32 v7, v118, v22
	v_fmac_f32_e32 v7, v119, v23
	s_waitcnt lgkmcnt(5)
	v_fmac_f32_e32 v8, v116, v24
	v_fmac_f32_e32 v8, v117, v25
	v_fmac_f32_e32 v8, v118, v26
	v_fmac_f32_e32 v8, v119, v27
	s_waitcnt lgkmcnt(4)
	v_fmac_f32_e32 v9, v116, v28
	v_fmac_f32_e32 v9, v117, v29
	v_fmac_f32_e32 v9, v118, v30
	v_fmac_f32_e32 v9, v119, v31
	s_waitcnt lgkmcnt(3)
	v_fmac_f32_e32 v10, v116, v32
	v_fmac_f32_e32 v10, v117, v33
	v_fmac_f32_e32 v10, v118, v34
	v_fmac_f32_e32 v10, v119, v35
	s_waitcnt lgkmcnt(2)
	v_fmac_f32_e32 v11, v116, v36
	v_fmac_f32_e32 v11, v117, v37
	v_fmac_f32_e32 v11, v118, v38
	v_fmac_f32_e32 v11, v119, v39
	s_waitcnt lgkmcnt(1)
	v_fmac_f32_e32 v4, v116, v40
	v_fmac_f32_e32 v4, v117, v41
	v_fmac_f32_e32 v4, v118, v42
	v_fmac_f32_e32 v4, v119, v43
	s_waitcnt lgkmcnt(0)
	v_fmac_f32_e32 v5, v116, v44
	v_fmac_f32_e32 v5, v117, v45
	v_fmac_f32_e32 v5, v118, v46
	v_fmac_f32_e32 v5, v119, v47
	ds_read_b128 v[16:19], v15 offset:96
	ds_read_b128 v[20:23], v15 offset:4192
	ds_read_b128 v[24:27], v15 offset:8288
	ds_read_b128 v[28:31], v15 offset:12384
	ds_read_b128 v[32:35], v15 offset:16480
	ds_read_b128 v[36:39], v15 offset:20576
	ds_read_b128 v[40:43], v15 offset:24672
	ds_read_b128 v[44:47], v15 offset:28768
	s_waitcnt lgkmcnt(7)
	v_fmac_f32_e32 v6, v120, v16
	v_fmac_f32_e32 v6, v121, v17
	v_fmac_f32_e32 v6, v122, v18
	v_fmac_f32_e32 v6, v123, v19
	s_waitcnt lgkmcnt(6)
	v_fmac_f32_e32 v7, v120, v20
	v_fmac_f32_e32 v7, v121, v21
	v_fmac_f32_e32 v7, v122, v22
	v_fmac_f32_e32 v7, v123, v23
	s_waitcnt lgkmcnt(5)
	v_fmac_f32_e32 v8, v120, v24
	v_fmac_f32_e32 v8, v121, v25
	v_fmac_f32_e32 v8, v122, v26
	v_fmac_f32_e32 v8, v123, v27
	s_waitcnt lgkmcnt(4)
	v_fmac_f32_e32 v9, v120, v28
	v_fmac_f32_e32 v9, v121, v29
	v_fmac_f32_e32 v9, v122, v30
	v_fmac_f32_e32 v9, v123, v31
	s_waitcnt lgkmcnt(3)
	v_fmac_f32_e32 v10, v120, v32
	v_fmac_f32_e32 v10, v121, v33
	v_fmac_f32_e32 v10, v122, v34
	v_fmac_f32_e32 v10, v123, v35
	s_waitcnt lgkmcnt(2)
; DI void phase_prologue(const Frame& F) {
;     ...
;         for (int k = 0; k < 128; ++k) { const float wv = wp[(size_t)k * 6144];
; #pragma unroll
;             for (int b = 0; b < 8; ++b) acc[b] += ca[b * D + kq * 128 + k] * wv; }
	v_fmac_f32_e32 v11, v120, v36
	v_fmac_f32_e32 v11, v121, v37
	v_fmac_f32_e32 v11, v122, v38
	v_fmac_f32_e32 v11, v123, v39
	s_waitcnt lgkmcnt(1)
	v_fmac_f32_e32 v4, v120, v40
	v_fmac_f32_e32 v4, v121, v41
	v_fmac_f32_e32 v4, v122, v42
	v_fmac_f32_e32 v4, v123, v43
	s_waitcnt lgkmcnt(0)
	v_fmac_f32_e32 v5, v120, v44
	v_fmac_f32_e32 v5, v121, v45
	v_fmac_f32_e32 v5, v122, v46
	v_fmac_f32_e32 v5, v123, v47
	ds_read_b128 v[16:19], v15 offset:112
	ds_read_b128 v[20:23], v15 offset:4208
	ds_read_b128 v[24:27], v15 offset:8304
	ds_read_b128 v[28:31], v15 offset:12400
	ds_read_b128 v[32:35], v15 offset:16496
	ds_read_b128 v[36:39], v15 offset:20592
	ds_read_b128 v[40:43], v15 offset:24688
	ds_read_b128 v[44:47], v15 offset:28784
	s_waitcnt lgkmcnt(7)
	v_fmac_f32_e32 v6, v124, v16
	v_fmac_f32_e32 v6, v125, v17
	v_fmac_f32_e32 v6, v126, v18
	v_fmac_f32_e32 v6, v127, v19
	s_waitcnt lgkmcnt(6)
	v_fmac_f32_e32 v7, v124, v20
	v_fmac_f32_e32 v7, v125, v21
	v_fmac_f32_e32 v7, v126, v22
	v_fmac_f32_e32 v7, v127, v23
	s_waitcnt lgkmcnt(5)
	v_fmac_f32_e32 v8, v124, v24
	v_fmac_f32_e32 v8, v125, v25
	v_fmac_f32_e32 v8, v126, v26
	v_fmac_f32_e32 v8, v127, v27
	s_waitcnt lgkmcnt(4)
	v_fmac_f32_e32 v9, v124, v28
	v_fmac_f32_e32 v9, v125, v29
	v_fmac_f32_e32 v9, v126, v30
	v_fmac_f32_e32 v9, v127, v31
	s_waitcnt lgkmcnt(3)
	v_fmac_f32_e32 v10, v124, v32
	v_fmac_f32_e32 v10, v125, v33
	v_fmac_f32_e32 v10, v126, v34
	v_fmac_f32_e32 v10, v127, v35
	s_waitcnt lgkmcnt(2)
	v_fmac_f32_e32 v11, v124, v36
	v_fmac_f32_e32 v11, v125, v37
	v_fmac_f32_e32 v11, v126, v38
	v_fmac_f32_e32 v11, v127, v39
	s_waitcnt lgkmcnt(1)
	v_fmac_f32_e32 v4, v124, v40
	v_fmac_f32_e32 v4, v125, v41
	v_fmac_f32_e32 v4, v126, v42
	v_fmac_f32_e32 v4, v127, v43
	s_waitcnt lgkmcnt(0)
	v_fmac_f32_e32 v5, v124, v44
	v_fmac_f32_e32 v5, v125, v45
	v_fmac_f32_e32 v5, v126, v46
	v_fmac_f32_e32 v5, v127, v47
	global_load_dword v112, v48, s[14:15]
	s_add_u32 s14, s14, 0x6000
	s_addc_u32 s15, s15, 0
	global_load_dword v113, v48, s[14:15]
	s_add_u32 s14, s14, 0x6000
	s_addc_u32 s15, s15, 0
	global_load_dword v114, v48, s[14:15]
	s_add_u32 s14, s14, 0x6000
	s_addc_u32 s15, s15, 0
	global_load_dword v115, v48, s[14:15]
	s_add_u32 s14, s14, 0x6000
	s_addc_u32 s15, s15, 0
	global_load_dword v116, v48, s[14:15]
	s_add_u32 s14, s14, 0x6000
	s_addc_u32 s15, s15, 0
	global_load_dword v117, v48, s[14:15]
	s_add_u32 s14, s14, 0x6000
	s_addc_u32 s15, s15, 0
	global_load_dword v118, v48, s[14:15]
	s_add_u32 s14, s14, 0x6000
	s_addc_u32 s15, s15, 0
	global_load_dword v119, v48, s[14:15]
	s_add_u32 s14, s14, 0x6000
	s_addc_u32 s15, s15, 0
	global_load_dword v120, v48, s[14:15]
	s_add_u32 s14, s14, 0x6000
	s_addc_u32 s15, s15, 0
	global_load_dword v121, v48, s[14:15]
	s_add_u32 s14, s14, 0x6000
	s_addc_u32 s15, s15, 0
	global_load_dword v122, v48, s[14:15]
	s_add_u32 s14, s14, 0x6000
	s_addc_u32 s15, s15, 0
	global_load_dword v123, v48, s[14:15]
	s_add_u32 s14, s14, 0x6000
	s_addc_u32 s15, s15, 0
	global_load_dword v124, v48, s[14:15]
	s_add_u32 s14, s14, 0x6000
	s_addc_u32 s15, s15, 0
	global_load_dword v125, v48, s[14:15]
	s_add_u32 s14, s14, 0x6000
	s_addc_u32 s15, s15, 0
	global_load_dword v126, v48, s[14:15]
	s_add_u32 s14, s14, 0x6000
	s_addc_u32 s15, s15, 0
	global_load_dword v127, v48, s[14:15]
	s_add_u32 s14, s14, 0x6000
	s_addc_u32 s15, s15, 0
	s_waitcnt vmcnt(48)
	ds_read_b128 v[16:19], v15 offset:128
	ds_read_b128 v[20:23], v15 offset:4224
	ds_read_b128 v[24:27], v15 offset:8320
	ds_read_b128 v[28:31], v15 offset:12416
	ds_read_b128 v[32:35], v15 offset:16512
	ds_read_b128 v[36:39], v15 offset:20608
	ds_read_b128 v[40:43], v15 offset:24704
	ds_read_b128 v[44:47], v15 offset:28800
	s_waitcnt lgkmcnt(7)
	v_fmac_f32_e32 v6, v149, v16
	v_fmac_f32_e32 v6, v150, v17
	v_fmac_f32_e32 v6, v151, v18
	v_fmac_f32_e32 v6, v152, v19
	s_waitcnt lgkmcnt(6)
	v_fmac_f32_e32 v7, v149, v20
	v_fmac_f32_e32 v7, v150, v21
	v_fmac_f32_e32 v7, v151, v22
	v_fmac_f32_e32 v7, v152, v23
	s_waitcnt lgkmcnt(5)
	v_fmac_f32_e32 v8, v149, v24
	v_fmac_f32_e32 v8, v150, v25
	v_fmac_f32_e32 v8, v151, v26
	v_fmac_f32_e32 v8, v152, v27
	s_waitcnt lgkmcnt(4)
	v_fmac_f32_e32 v9, v149, v28
	v_fmac_f32_e32 v9, v150, v29
	v_fmac_f32_e32 v9, v151, v30
	v_fmac_f32_e32 v9, v152, v31
	s_waitcnt lgkmcnt(3)
	v_fmac_f32_e32 v10, v149, v32
	v_fmac_f32_e32 v10, v150, v33
	v_fmac_f32_e32 v10, v151, v34
	v_fmac_f32_e32 v10, v152, v35
	s_waitcnt lgkmcnt(2)
	v_fmac_f32_e32 v11, v149, v36
	v_fmac_f32_e32 v11, v150, v37
	v_fmac_f32_e32 v11, v151, v38
	v_fmac_f32_e32 v11, v152, v39
	s_waitcnt lgkmcnt(1)
	v_fmac_f32_e32 v4, v149, v40
	v_fmac_f32_e32 v4, v150, v41
	v_fmac_f32_e32 v4, v151, v42
	v_fmac_f32_e32 v4, v152, v43
	s_waitcnt lgkmcnt(0)
	v_fmac_f32_e32 v5, v149, v44
	v_fmac_f32_e32 v5, v150, v45
	v_fmac_f32_e32 v5, v151, v46
	v_fmac_f32_e32 v5, v152, v47
	ds_read_b128 v[16:19], v15 offset:144
	ds_read_b128 v[20:23], v15 offset:4240
	ds_read_b128 v[24:27], v15 offset:8336
	ds_read_b128 v[28:31], v15 offset:12432
	ds_read_b128 v[32:35], v15 offset:16528
	ds_read_b128 v[36:39], v15 offset:20624
	ds_read_b128 v[40:43], v15 offset:24720
	ds_read_b128 v[44:47], v15 offset:28816
	s_waitcnt lgkmcnt(7)
	v_fmac_f32_e32 v6, v153, v16
	v_fmac_f32_e32 v6, v154, v17
	v_fmac_f32_e32 v6, v155, v18
	v_fmac_f32_e32 v6, v156, v19
	s_waitcnt lgkmcnt(6)
	v_fmac_f32_e32 v7, v153, v20
	v_fmac_f32_e32 v7, v154, v21
	v_fmac_f32_e32 v7, v155, v22
	v_fmac_f32_e32 v7, v156, v23
	s_waitcnt lgkmcnt(5)
	v_fmac_f32_e32 v8, v153, v24
	v_fmac_f32_e32 v8, v154, v25
	v_fmac_f32_e32 v8, v155, v26
	v_fmac_f32_e32 v8, v156, v27
	s_waitcnt lgkmcnt(4)
; DI void phase_prologue(const Frame& F) {
;     ...
;         for (int k = 0; k < 128; ++k) { const float wv = wp[(size_t)k * 6144];
; #pragma unroll
;             for (int b = 0; b < 8; ++b) acc[b] += ca[b * D + kq * 128 + k] * wv; }
	v_fmac_f32_e32 v9, v153, v28
	v_fmac_f32_e32 v9, v154, v29
	v_fmac_f32_e32 v9, v155, v30
	v_fmac_f32_e32 v9, v156, v31
	s_waitcnt lgkmcnt(3)
	v_fmac_f32_e32 v10, v153, v32
	v_fmac_f32_e32 v10, v154, v33
	v_fmac_f32_e32 v10, v155, v34
	v_fmac_f32_e32 v10, v156, v35
	s_waitcnt lgkmcnt(2)
	v_fmac_f32_e32 v11, v153, v36
	v_fmac_f32_e32 v11, v154, v37
	v_fmac_f32_e32 v11, v155, v38
	v_fmac_f32_e32 v11, v156, v39
	s_waitcnt lgkmcnt(1)
	v_fmac_f32_e32 v4, v153, v40
	v_fmac_f32_e32 v4, v154, v41
	v_fmac_f32_e32 v4, v155, v42
	v_fmac_f32_e32 v4, v156, v43
	s_waitcnt lgkmcnt(0)
	v_fmac_f32_e32 v5, v153, v44
	v_fmac_f32_e32 v5, v154, v45
	v_fmac_f32_e32 v5, v155, v46
	v_fmac_f32_e32 v5, v156, v47
	ds_read_b128 v[16:19], v15 offset:160
	ds_read_b128 v[20:23], v15 offset:4256
	ds_read_b128 v[24:27], v15 offset:8352
	ds_read_b128 v[28:31], v15 offset:12448
	ds_read_b128 v[32:35], v15 offset:16544
	ds_read_b128 v[36:39], v15 offset:20640
	ds_read_b128 v[40:43], v15 offset:24736
	ds_read_b128 v[44:47], v15 offset:28832
	s_waitcnt lgkmcnt(7)
	v_fmac_f32_e32 v6, v157, v16
	v_fmac_f32_e32 v6, v158, v17
	v_fmac_f32_e32 v6, v159, v18
	v_fmac_f32_e32 v6, v160, v19
	s_waitcnt lgkmcnt(6)
	v_fmac_f32_e32 v7, v157, v20
	v_fmac_f32_e32 v7, v158, v21
	v_fmac_f32_e32 v7, v159, v22
	v_fmac_f32_e32 v7, v160, v23
	s_waitcnt lgkmcnt(5)
	v_fmac_f32_e32 v8, v157, v24
	v_fmac_f32_e32 v8, v158, v25
	v_fmac_f32_e32 v8, v159, v26
	v_fmac_f32_e32 v8, v160, v27
	s_waitcnt lgkmcnt(4)
	v_fmac_f32_e32 v9, v157, v28
	v_fmac_f32_e32 v9, v158, v29
	v_fmac_f32_e32 v9, v159, v30
	v_fmac_f32_e32 v9, v160, v31
	s_waitcnt lgkmcnt(3)
	v_fmac_f32_e32 v10, v157, v32
	v_fmac_f32_e32 v10, v158, v33
	v_fmac_f32_e32 v10, v159, v34
	v_fmac_f32_e32 v10, v160, v35
	s_waitcnt lgkmcnt(2)
	v_fmac_f32_e32 v11, v157, v36
	v_fmac_f32_e32 v11, v158, v37
	v_fmac_f32_e32 v11, v159, v38
	v_fmac_f32_e32 v11, v160, v39
	s_waitcnt lgkmcnt(1)
	v_fmac_f32_e32 v4, v157, v40
	v_fmac_f32_e32 v4, v158, v41
	v_fmac_f32_e32 v4, v159, v42
	v_fmac_f32_e32 v4, v160, v43
	s_waitcnt lgkmcnt(0)
	v_fmac_f32_e32 v5, v157, v44
	v_fmac_f32_e32 v5, v158, v45
	v_fmac_f32_e32 v5, v159, v46
	v_fmac_f32_e32 v5, v160, v47
	ds_read_b128 v[16:19], v15 offset:176
	ds_read_b128 v[20:23], v15 offset:4272
	ds_read_b128 v[24:27], v15 offset:8368
	ds_read_b128 v[28:31], v15 offset:12464
	ds_read_b128 v[32:35], v15 offset:16560
	ds_read_b128 v[36:39], v15 offset:20656
	ds_read_b128 v[40:43], v15 offset:24752
	ds_read_b128 v[44:47], v15 offset:28848
	s_waitcnt lgkmcnt(7)
	v_fmac_f32_e32 v6, v161, v16
	v_fmac_f32_e32 v6, v162, v17
	v_fmac_f32_e32 v6, v163, v18
	v_fmac_f32_e32 v6, v164, v19
	s_waitcnt lgkmcnt(6)
	v_fmac_f32_e32 v7, v161, v20
	v_fmac_f32_e32 v7, v162, v21
	v_fmac_f32_e32 v7, v163, v22
	v_fmac_f32_e32 v7, v164, v23
	s_waitcnt lgkmcnt(5)
	v_fmac_f32_e32 v8, v161, v24
	v_fmac_f32_e32 v8, v162, v25
	v_fmac_f32_e32 v8, v163, v26
	v_fmac_f32_e32 v8, v164, v27
	s_waitcnt lgkmcnt(4)
	v_fmac_f32_e32 v9, v161, v28
	v_fmac_f32_e32 v9, v162, v29
	v_fmac_f32_e32 v9, v163, v30
	v_fmac_f32_e32 v9, v164, v31
	s_waitcnt lgkmcnt(3)
	v_fmac_f32_e32 v10, v161, v32
	v_fmac_f32_e32 v10, v162, v33
	v_fmac_f32_e32 v10, v163, v34
	v_fmac_f32_e32 v10, v164, v35
	s_waitcnt lgkmcnt(2)
	v_fmac_f32_e32 v11, v161, v36
	v_fmac_f32_e32 v11, v162, v37
	v_fmac_f32_e32 v11, v163, v38
	v_fmac_f32_e32 v11, v164, v39
	s_waitcnt lgkmcnt(1)
	v_fmac_f32_e32 v4, v161, v40
	v_fmac_f32_e32 v4, v162, v41
	v_fmac_f32_e32 v4, v163, v42
	v_fmac_f32_e32 v4, v164, v43
	s_waitcnt lgkmcnt(0)
	v_fmac_f32_e32 v5, v161, v44
	v_fmac_f32_e32 v5, v162, v45
	v_fmac_f32_e32 v5, v163, v46
	v_fmac_f32_e32 v5, v164, v47
	global_load_dword v149, v48, s[14:15]
	s_add_u32 s14, s14, 0x6000
	s_addc_u32 s15, s15, 0
	global_load_dword v150, v48, s[14:15]
	s_add_u32 s14, s14, 0x6000
	s_addc_u32 s15, s15, 0
	global_load_dword v151, v48, s[14:15]
	s_add_u32 s14, s14, 0x6000
	s_addc_u32 s15, s15, 0
	global_load_dword v152, v48, s[14:15]
	s_add_u32 s14, s14, 0x6000
	s_addc_u32 s15, s15, 0
	global_load_dword v153, v48, s[14:15]
	s_add_u32 s14, s14, 0x6000
	s_addc_u32 s15, s15, 0
	global_load_dword v154, v48, s[14:15]
	s_add_u32 s14, s14, 0x6000
	s_addc_u32 s15, s15, 0
	global_load_dword v155, v48, s[14:15]
	s_add_u32 s14, s14, 0x6000
	s_addc_u32 s15, s15, 0
	global_load_dword v156, v48, s[14:15]
	s_add_u32 s14, s14, 0x6000
	s_addc_u32 s15, s15, 0
	global_load_dword v157, v48, s[14:15]
	s_add_u32 s14, s14, 0x6000
	s_addc_u32 s15, s15, 0
	global_load_dword v158, v48, s[14:15]
	s_add_u32 s14, s14, 0x6000
	s_addc_u32 s15, s15, 0
	global_load_dword v159, v48, s[14:15]
	s_add_u32 s14, s14, 0x6000
	s_addc_u32 s15, s15, 0
	global_load_dword v160, v48, s[14:15]
	s_add_u32 s14, s14, 0x6000
	s_addc_u32 s15, s15, 0
	global_load_dword v161, v48, s[14:15]
	s_add_u32 s14, s14, 0x6000
	s_addc_u32 s15, s15, 0
	global_load_dword v162, v48, s[14:15]
	s_add_u32 s14, s14, 0x6000
	s_addc_u32 s15, s15, 0
	global_load_dword v163, v48, s[14:15]
	s_add_u32 s14, s14, 0x6000
	s_addc_u32 s15, s15, 0
	global_load_dword v164, v48, s[14:15]
	s_add_u32 s14, s14, 0x6000
	s_addc_u32 s15, s15, 0
	s_waitcnt vmcnt(48)
	ds_read_b128 v[16:19], v15 offset:192
	ds_read_b128 v[20:23], v15 offset:4288
	ds_read_b128 v[24:27], v15 offset:8384
	ds_read_b128 v[28:31], v15 offset:12480
	ds_read_b128 v[32:35], v15 offset:16576
	ds_read_b128 v[36:39], v15 offset:20672
	ds_read_b128 v[40:43], v15 offset:24768
	ds_read_b128 v[44:47], v15 offset:28864
	s_waitcnt lgkmcnt(7)
	v_fmac_f32_e32 v6, v165, v16
	v_fmac_f32_e32 v6, v166, v17
	v_fmac_f32_e32 v6, v167, v18
	v_fmac_f32_e32 v6, v168, v19
	s_waitcnt lgkmcnt(6)
; DI void phase_prologue(const Frame& F) {
;     ...
;         for (int k = 0; k < 128; ++k) { const float wv = wp[(size_t)k * 6144];
; #pragma unroll
;             for (int b = 0; b < 8; ++b) acc[b] += ca[b * D + kq * 128 + k] * wv; }
	v_fmac_f32_e32 v7, v165, v20
	v_fmac_f32_e32 v7, v166, v21
	v_fmac_f32_e32 v7, v167, v22
	v_fmac_f32_e32 v7, v168, v23
	s_waitcnt lgkmcnt(5)
	v_fmac_f32_e32 v8, v165, v24
	v_fmac_f32_e32 v8, v166, v25
	v_fmac_f32_e32 v8, v167, v26
	v_fmac_f32_e32 v8, v168, v27
	s_waitcnt lgkmcnt(4)
	v_fmac_f32_e32 v9, v165, v28
	v_fmac_f32_e32 v9, v166, v29
	v_fmac_f32_e32 v9, v167, v30
	v_fmac_f32_e32 v9, v168, v31
	s_waitcnt lgkmcnt(3)
	v_fmac_f32_e32 v10, v165, v32
	v_fmac_f32_e32 v10, v166, v33
	v_fmac_f32_e32 v10, v167, v34
	v_fmac_f32_e32 v10, v168, v35
	s_waitcnt lgkmcnt(2)
	v_fmac_f32_e32 v11, v165, v36
	v_fmac_f32_e32 v11, v166, v37
	v_fmac_f32_e32 v11, v167, v38
	v_fmac_f32_e32 v11, v168, v39
	s_waitcnt lgkmcnt(1)
	v_fmac_f32_e32 v4, v165, v40
	v_fmac_f32_e32 v4, v166, v41
	v_fmac_f32_e32 v4, v167, v42
	v_fmac_f32_e32 v4, v168, v43
	s_waitcnt lgkmcnt(0)
	v_fmac_f32_e32 v5, v165, v44
	v_fmac_f32_e32 v5, v166, v45
	v_fmac_f32_e32 v5, v167, v46
	v_fmac_f32_e32 v5, v168, v47
	ds_read_b128 v[16:19], v15 offset:208
	ds_read_b128 v[20:23], v15 offset:4304
	ds_read_b128 v[24:27], v15 offset:8400
	ds_read_b128 v[28:31], v15 offset:12496
	ds_read_b128 v[32:35], v15 offset:16592
	ds_read_b128 v[36:39], v15 offset:20688
	ds_read_b128 v[40:43], v15 offset:24784
	ds_read_b128 v[44:47], v15 offset:28880
	s_waitcnt lgkmcnt(7)
	v_fmac_f32_e32 v6, v169, v16
	v_fmac_f32_e32 v6, v170, v17
	v_fmac_f32_e32 v6, v171, v18
	v_fmac_f32_e32 v6, v172, v19
	s_waitcnt lgkmcnt(6)
	v_fmac_f32_e32 v7, v169, v20
	v_fmac_f32_e32 v7, v170, v21
	v_fmac_f32_e32 v7, v171, v22
	v_fmac_f32_e32 v7, v172, v23
	s_waitcnt lgkmcnt(5)
	v_fmac_f32_e32 v8, v169, v24
	v_fmac_f32_e32 v8, v170, v25
	v_fmac_f32_e32 v8, v171, v26
	v_fmac_f32_e32 v8, v172, v27
	s_waitcnt lgkmcnt(4)
	v_fmac_f32_e32 v9, v169, v28
	v_fmac_f32_e32 v9, v170, v29
	v_fmac_f32_e32 v9, v171, v30
	v_fmac_f32_e32 v9, v172, v31
	s_waitcnt lgkmcnt(3)
	v_fmac_f32_e32 v10, v169, v32
	v_fmac_f32_e32 v10, v170, v33
	v_fmac_f32_e32 v10, v171, v34
	v_fmac_f32_e32 v10, v172, v35
	s_waitcnt lgkmcnt(2)
	v_fmac_f32_e32 v11, v169, v36
	v_fmac_f32_e32 v11, v170, v37
	v_fmac_f32_e32 v11, v171, v38
	v_fmac_f32_e32 v11, v172, v39
	s_waitcnt lgkmcnt(1)
	v_fmac_f32_e32 v4, v169, v40
	v_fmac_f32_e32 v4, v170, v41
	v_fmac_f32_e32 v4, v171, v42
	v_fmac_f32_e32 v4, v172, v43
	s_waitcnt lgkmcnt(0)
	v_fmac_f32_e32 v5, v169, v44
	v_fmac_f32_e32 v5, v170, v45
	v_fmac_f32_e32 v5, v171, v46
	v_fmac_f32_e32 v5, v172, v47
	ds_read_b128 v[16:19], v15 offset:224
	ds_read_b128 v[20:23], v15 offset:4320
	ds_read_b128 v[24:27], v15 offset:8416
	ds_read_b128 v[28:31], v15 offset:12512
	ds_read_b128 v[32:35], v15 offset:16608
	ds_read_b128 v[36:39], v15 offset:20704
	ds_read_b128 v[40:43], v15 offset:24800
	ds_read_b128 v[44:47], v15 offset:28896
	s_waitcnt lgkmcnt(7)
	v_fmac_f32_e32 v6, v173, v16
	v_fmac_f32_e32 v6, v174, v17
	v_fmac_f32_e32 v6, v175, v18
	v_fmac_f32_e32 v6, v176, v19
	s_waitcnt lgkmcnt(6)
	v_fmac_f32_e32 v7, v173, v20
	v_fmac_f32_e32 v7, v174, v21
	v_fmac_f32_e32 v7, v175, v22
	v_fmac_f32_e32 v7, v176, v23
	s_waitcnt lgkmcnt(5)
	v_fmac_f32_e32 v8, v173, v24
	v_fmac_f32_e32 v8, v174, v25
	v_fmac_f32_e32 v8, v175, v26
	v_fmac_f32_e32 v8, v176, v27
	s_waitcnt lgkmcnt(4)
	v_fmac_f32_e32 v9, v173, v28
	v_fmac_f32_e32 v9, v174, v29
	v_fmac_f32_e32 v9, v175, v30
	v_fmac_f32_e32 v9, v176, v31
	s_waitcnt lgkmcnt(3)
	v_fmac_f32_e32 v10, v173, v32
	v_fmac_f32_e32 v10, v174, v33
	v_fmac_f32_e32 v10, v175, v34
	v_fmac_f32_e32 v10, v176, v35
	s_waitcnt lgkmcnt(2)
	v_fmac_f32_e32 v11, v173, v36
	v_fmac_f32_e32 v11, v174, v37
	v_fmac_f32_e32 v11, v175, v38
	v_fmac_f32_e32 v11, v176, v39
	s_waitcnt lgkmcnt(1)
	v_fmac_f32_e32 v4, v173, v40
	v_fmac_f32_e32 v4, v174, v41
	v_fmac_f32_e32 v4, v175, v42
	v_fmac_f32_e32 v4, v176, v43
	s_waitcnt lgkmcnt(0)
	v_fmac_f32_e32 v5, v173, v44
	v_fmac_f32_e32 v5, v174, v45
	v_fmac_f32_e32 v5, v175, v46
	v_fmac_f32_e32 v5, v176, v47
	ds_read_b128 v[16:19], v15 offset:240
	ds_read_b128 v[20:23], v15 offset:4336
	ds_read_b128 v[24:27], v15 offset:8432
	ds_read_b128 v[28:31], v15 offset:12528
	ds_read_b128 v[32:35], v15 offset:16624
	ds_read_b128 v[36:39], v15 offset:20720
	ds_read_b128 v[40:43], v15 offset:24816
	ds_read_b128 v[44:47], v15 offset:28912
	s_waitcnt lgkmcnt(7)
	v_fmac_f32_e32 v6, v177, v16
	v_fmac_f32_e32 v6, v178, v17
	v_fmac_f32_e32 v6, v179, v18
	v_fmac_f32_e32 v6, v180, v19
	s_waitcnt lgkmcnt(6)
	v_fmac_f32_e32 v7, v177, v20
	v_fmac_f32_e32 v7, v178, v21
	v_fmac_f32_e32 v7, v179, v22
	v_fmac_f32_e32 v7, v180, v23
	s_waitcnt lgkmcnt(5)
	v_fmac_f32_e32 v8, v177, v24
	v_fmac_f32_e32 v8, v178, v25
	v_fmac_f32_e32 v8, v179, v26
	v_fmac_f32_e32 v8, v180, v27
	s_waitcnt lgkmcnt(4)
	v_fmac_f32_e32 v9, v177, v28
	v_fmac_f32_e32 v9, v178, v29
	v_fmac_f32_e32 v9, v179, v30
	v_fmac_f32_e32 v9, v180, v31
	s_waitcnt lgkmcnt(3)
	v_fmac_f32_e32 v10, v177, v32
	v_fmac_f32_e32 v10, v178, v33
	v_fmac_f32_e32 v10, v179, v34
	v_fmac_f32_e32 v10, v180, v35
	s_waitcnt lgkmcnt(2)
	v_fmac_f32_e32 v11, v177, v36
	v_fmac_f32_e32 v11, v178, v37
	v_fmac_f32_e32 v11, v179, v38
	v_fmac_f32_e32 v11, v180, v39
	s_waitcnt lgkmcnt(1)
	v_fmac_f32_e32 v4, v177, v40
	v_fmac_f32_e32 v4, v178, v41
	v_fmac_f32_e32 v4, v179, v42
	v_fmac_f32_e32 v4, v180, v43
	s_waitcnt lgkmcnt(0)
; DI void phase_prologue(const Frame& F) {
;     ...
;         for (int k = 0; k < 128; ++k) { const float wv = wp[(size_t)k * 6144];
; #pragma unroll
;             for (int b = 0; b < 8; ++b) acc[b] += ca[b * D + kq * 128 + k] * wv; }
	v_fmac_f32_e32 v5, v177, v44
	v_fmac_f32_e32 v5, v178, v45
	v_fmac_f32_e32 v5, v179, v46
	v_fmac_f32_e32 v5, v180, v47
	global_load_dword v165, v48, s[14:15]
	s_add_u32 s14, s14, 0x6000
	s_addc_u32 s15, s15, 0
	global_load_dword v166, v48, s[14:15]
	s_add_u32 s14, s14, 0x6000
	s_addc_u32 s15, s15, 0
	global_load_dword v167, v48, s[14:15]
	s_add_u32 s14, s14, 0x6000
	s_addc_u32 s15, s15, 0
	global_load_dword v168, v48, s[14:15]
	s_add_u32 s14, s14, 0x6000
	s_addc_u32 s15, s15, 0
	global_load_dword v169, v48, s[14:15]
	s_add_u32 s14, s14, 0x6000
	s_addc_u32 s15, s15, 0
	global_load_dword v170, v48, s[14:15]
	s_add_u32 s14, s14, 0x6000
	s_addc_u32 s15, s15, 0
	global_load_dword v171, v48, s[14:15]
	s_add_u32 s14, s14, 0x6000
	s_addc_u32 s15, s15, 0
	global_load_dword v172, v48, s[14:15]
	s_add_u32 s14, s14, 0x6000
	s_addc_u32 s15, s15, 0
	global_load_dword v173, v48, s[14:15]
	s_add_u32 s14, s14, 0x6000
	s_addc_u32 s15, s15, 0
	global_load_dword v174, v48, s[14:15]
	s_add_u32 s14, s14, 0x6000
	s_addc_u32 s15, s15, 0
	global_load_dword v175, v48, s[14:15]
	s_add_u32 s14, s14, 0x6000
	s_addc_u32 s15, s15, 0
	global_load_dword v176, v48, s[14:15]
	s_add_u32 s14, s14, 0x6000
	s_addc_u32 s15, s15, 0
	global_load_dword v177, v48, s[14:15]
	s_add_u32 s14, s14, 0x6000
	s_addc_u32 s15, s15, 0
	global_load_dword v178, v48, s[14:15]
	s_add_u32 s14, s14, 0x6000
	s_addc_u32 s15, s15, 0
	global_load_dword v179, v48, s[14:15]
	s_add_u32 s14, s14, 0x6000
	s_addc_u32 s15, s15, 0
	global_load_dword v180, v48, s[14:15]
	s_add_u32 s14, s14, 0x6000
	s_addc_u32 s15, s15, 0
	s_waitcnt vmcnt(48)
	ds_read_b128 v[16:19], v15 offset:256
	ds_read_b128 v[20:23], v15 offset:4352
	ds_read_b128 v[24:27], v15 offset:8448
	ds_read_b128 v[28:31], v15 offset:12544
	ds_read_b128 v[32:35], v15 offset:16640
	ds_read_b128 v[36:39], v15 offset:20736
	ds_read_b128 v[40:43], v15 offset:24832
	ds_read_b128 v[44:47], v15 offset:28928
	s_waitcnt lgkmcnt(7)
	v_fmac_f32_e32 v6, v64, v16
	v_fmac_f32_e32 v6, v65, v17
	v_fmac_f32_e32 v6, v66, v18
	v_fmac_f32_e32 v6, v67, v19
	s_waitcnt lgkmcnt(6)
	v_fmac_f32_e32 v7, v64, v20
	v_fmac_f32_e32 v7, v65, v21
	v_fmac_f32_e32 v7, v66, v22
	v_fmac_f32_e32 v7, v67, v23
	s_waitcnt lgkmcnt(5)
	v_fmac_f32_e32 v8, v64, v24
	v_fmac_f32_e32 v8, v65, v25
	v_fmac_f32_e32 v8, v66, v26
	v_fmac_f32_e32 v8, v67, v27
	s_waitcnt lgkmcnt(4)
	v_fmac_f32_e32 v9, v64, v28
	v_fmac_f32_e32 v9, v65, v29
	v_fmac_f32_e32 v9, v66, v30
	v_fmac_f32_e32 v9, v67, v31
	s_waitcnt lgkmcnt(3)
	v_fmac_f32_e32 v10, v64, v32
	v_fmac_f32_e32 v10, v65, v33
	v_fmac_f32_e32 v10, v66, v34
	v_fmac_f32_e32 v10, v67, v35
	s_waitcnt lgkmcnt(2)
	v_fmac_f32_e32 v11, v64, v36
	v_fmac_f32_e32 v11, v65, v37
	v_fmac_f32_e32 v11, v66, v38
	v_fmac_f32_e32 v11, v67, v39
	s_waitcnt lgkmcnt(1)
	v_fmac_f32_e32 v4, v64, v40
	v_fmac_f32_e32 v4, v65, v41
	v_fmac_f32_e32 v4, v66, v42
	v_fmac_f32_e32 v4, v67, v43
	s_waitcnt lgkmcnt(0)
	v_fmac_f32_e32 v5, v64, v44
	v_fmac_f32_e32 v5, v65, v45
	v_fmac_f32_e32 v5, v66, v46
	v_fmac_f32_e32 v5, v67, v47
	ds_read_b128 v[16:19], v15 offset:272
	ds_read_b128 v[20:23], v15 offset:4368
	ds_read_b128 v[24:27], v15 offset:8464
	ds_read_b128 v[28:31], v15 offset:12560
	ds_read_b128 v[32:35], v15 offset:16656
	ds_read_b128 v[36:39], v15 offset:20752
	ds_read_b128 v[40:43], v15 offset:24848
	ds_read_b128 v[44:47], v15 offset:28944
	s_waitcnt lgkmcnt(7)
	v_fmac_f32_e32 v6, v68, v16
	v_fmac_f32_e32 v6, v69, v17
	v_fmac_f32_e32 v6, v70, v18
	v_fmac_f32_e32 v6, v71, v19
	s_waitcnt lgkmcnt(6)
	v_fmac_f32_e32 v7, v68, v20
	v_fmac_f32_e32 v7, v69, v21
	v_fmac_f32_e32 v7, v70, v22
	v_fmac_f32_e32 v7, v71, v23
	s_waitcnt lgkmcnt(5)
	v_fmac_f32_e32 v8, v68, v24
	v_fmac_f32_e32 v8, v69, v25
	v_fmac_f32_e32 v8, v70, v26
	v_fmac_f32_e32 v8, v71, v27
	s_waitcnt lgkmcnt(4)
	v_fmac_f32_e32 v9, v68, v28
	v_fmac_f32_e32 v9, v69, v29
	v_fmac_f32_e32 v9, v70, v30
	v_fmac_f32_e32 v9, v71, v31
	s_waitcnt lgkmcnt(3)
	v_fmac_f32_e32 v10, v68, v32
	v_fmac_f32_e32 v10, v69, v33
	v_fmac_f32_e32 v10, v70, v34
	v_fmac_f32_e32 v10, v71, v35
	s_waitcnt lgkmcnt(2)
	v_fmac_f32_e32 v11, v68, v36
	v_fmac_f32_e32 v11, v69, v37
	v_fmac_f32_e32 v11, v70, v38
	v_fmac_f32_e32 v11, v71, v39
	s_waitcnt lgkmcnt(1)
	v_fmac_f32_e32 v4, v68, v40
	v_fmac_f32_e32 v4, v69, v41
	v_fmac_f32_e32 v4, v70, v42
	v_fmac_f32_e32 v4, v71, v43
	s_waitcnt lgkmcnt(0)
	v_fmac_f32_e32 v5, v68, v44
	v_fmac_f32_e32 v5, v69, v45
	v_fmac_f32_e32 v5, v70, v46
	v_fmac_f32_e32 v5, v71, v47
	ds_read_b128 v[16:19], v15 offset:288
	ds_read_b128 v[20:23], v15 offset:4384
	ds_read_b128 v[24:27], v15 offset:8480
	ds_read_b128 v[28:31], v15 offset:12576
	ds_read_b128 v[32:35], v15 offset:16672
	ds_read_b128 v[36:39], v15 offset:20768
	ds_read_b128 v[40:43], v15 offset:24864
	ds_read_b128 v[44:47], v15 offset:28960
	s_waitcnt lgkmcnt(7)
	v_fmac_f32_e32 v6, v72, v16
	v_fmac_f32_e32 v6, v73, v17
	v_fmac_f32_e32 v6, v74, v18
	v_fmac_f32_e32 v6, v75, v19
	s_waitcnt lgkmcnt(6)
	v_fmac_f32_e32 v7, v72, v20
	v_fmac_f32_e32 v7, v73, v21
	v_fmac_f32_e32 v7, v74, v22
	v_fmac_f32_e32 v7, v75, v23
	s_waitcnt lgkmcnt(5)
	v_fmac_f32_e32 v8, v72, v24
	v_fmac_f32_e32 v8, v73, v25
	v_fmac_f32_e32 v8, v74, v26
	v_fmac_f32_e32 v8, v75, v27
	s_waitcnt lgkmcnt(4)
	v_fmac_f32_e32 v9, v72, v28
	v_fmac_f32_e32 v9, v73, v29
	v_fmac_f32_e32 v9, v74, v30
	v_fmac_f32_e32 v9, v75, v31
	s_waitcnt lgkmcnt(3)
	v_fmac_f32_e32 v10, v72, v32
	v_fmac_f32_e32 v10, v73, v33
	v_fmac_f32_e32 v10, v74, v34
	v_fmac_f32_e32 v10, v75, v35
	s_waitcnt lgkmcnt(2)
	v_fmac_f32_e32 v11, v72, v36
	v_fmac_f32_e32 v11, v73, v37
	v_fmac_f32_e32 v11, v74, v38
	v_fmac_f32_e32 v11, v75, v39
	s_waitcnt lgkmcnt(1)
; DI void phase_prologue(const Frame& F) {
;     ...
;         for (int k = 0; k < 128; ++k) { const float wv = wp[(size_t)k * 6144];
; #pragma unroll
;             for (int b = 0; b < 8; ++b) acc[b] += ca[b * D + kq * 128 + k] * wv; }
	v_fmac_f32_e32 v4, v72, v40
	v_fmac_f32_e32 v4, v73, v41
	v_fmac_f32_e32 v4, v74, v42
	v_fmac_f32_e32 v4, v75, v43
	s_waitcnt lgkmcnt(0)
	v_fmac_f32_e32 v5, v72, v44
	v_fmac_f32_e32 v5, v73, v45
	v_fmac_f32_e32 v5, v74, v46
	v_fmac_f32_e32 v5, v75, v47
	ds_read_b128 v[16:19], v15 offset:304
	ds_read_b128 v[20:23], v15 offset:4400
	ds_read_b128 v[24:27], v15 offset:8496
	ds_read_b128 v[28:31], v15 offset:12592
	ds_read_b128 v[32:35], v15 offset:16688
	ds_read_b128 v[36:39], v15 offset:20784
	ds_read_b128 v[40:43], v15 offset:24880
	ds_read_b128 v[44:47], v15 offset:28976
	s_waitcnt lgkmcnt(7)
	v_fmac_f32_e32 v6, v76, v16
	v_fmac_f32_e32 v6, v77, v17
	v_fmac_f32_e32 v6, v78, v18
	v_fmac_f32_e32 v6, v79, v19
	s_waitcnt lgkmcnt(6)
	v_fmac_f32_e32 v7, v76, v20
	v_fmac_f32_e32 v7, v77, v21
	v_fmac_f32_e32 v7, v78, v22
	v_fmac_f32_e32 v7, v79, v23
	s_waitcnt lgkmcnt(5)
	v_fmac_f32_e32 v8, v76, v24
	v_fmac_f32_e32 v8, v77, v25
	v_fmac_f32_e32 v8, v78, v26
	v_fmac_f32_e32 v8, v79, v27
	s_waitcnt lgkmcnt(4)
	v_fmac_f32_e32 v9, v76, v28
	v_fmac_f32_e32 v9, v77, v29
	v_fmac_f32_e32 v9, v78, v30
	v_fmac_f32_e32 v9, v79, v31
	s_waitcnt lgkmcnt(3)
	v_fmac_f32_e32 v10, v76, v32
	v_fmac_f32_e32 v10, v77, v33
	v_fmac_f32_e32 v10, v78, v34
	v_fmac_f32_e32 v10, v79, v35
	s_waitcnt lgkmcnt(2)
	v_fmac_f32_e32 v11, v76, v36
	v_fmac_f32_e32 v11, v77, v37
	v_fmac_f32_e32 v11, v78, v38
	v_fmac_f32_e32 v11, v79, v39
	s_waitcnt lgkmcnt(1)
	v_fmac_f32_e32 v4, v76, v40
	v_fmac_f32_e32 v4, v77, v41
	v_fmac_f32_e32 v4, v78, v42
	v_fmac_f32_e32 v4, v79, v43
	s_waitcnt lgkmcnt(0)
	v_fmac_f32_e32 v5, v76, v44
	v_fmac_f32_e32 v5, v77, v45
	v_fmac_f32_e32 v5, v78, v46
	v_fmac_f32_e32 v5, v79, v47
	s_waitcnt vmcnt(32)
	ds_read_b128 v[16:19], v15 offset:320
	ds_read_b128 v[20:23], v15 offset:4416
	ds_read_b128 v[24:27], v15 offset:8512
	ds_read_b128 v[28:31], v15 offset:12608
	ds_read_b128 v[32:35], v15 offset:16704
	ds_read_b128 v[36:39], v15 offset:20800
	ds_read_b128 v[40:43], v15 offset:24896
	ds_read_b128 v[44:47], v15 offset:28992
	s_waitcnt lgkmcnt(7)
	v_fmac_f32_e32 v6, v112, v16
	v_fmac_f32_e32 v6, v113, v17
	v_fmac_f32_e32 v6, v114, v18
	v_fmac_f32_e32 v6, v115, v19
	s_waitcnt lgkmcnt(6)
	v_fmac_f32_e32 v7, v112, v20
	v_fmac_f32_e32 v7, v113, v21
	v_fmac_f32_e32 v7, v114, v22
	v_fmac_f32_e32 v7, v115, v23
	s_waitcnt lgkmcnt(5)
	v_fmac_f32_e32 v8, v112, v24
	v_fmac_f32_e32 v8, v113, v25
	v_fmac_f32_e32 v8, v114, v26
	v_fmac_f32_e32 v8, v115, v27
	s_waitcnt lgkmcnt(4)
	v_fmac_f32_e32 v9, v112, v28
	v_fmac_f32_e32 v9, v113, v29
	v_fmac_f32_e32 v9, v114, v30
	v_fmac_f32_e32 v9, v115, v31
	s_waitcnt lgkmcnt(3)
	v_fmac_f32_e32 v10, v112, v32
	v_fmac_f32_e32 v10, v113, v33
	v_fmac_f32_e32 v10, v114, v34
	v_fmac_f32_e32 v10, v115, v35
	s_waitcnt lgkmcnt(2)
	v_fmac_f32_e32 v11, v112, v36
	v_fmac_f32_e32 v11, v113, v37
	v_fmac_f32_e32 v11, v114, v38
	v_fmac_f32_e32 v11, v115, v39
	s_waitcnt lgkmcnt(1)
	v_fmac_f32_e32 v4, v112, v40
	v_fmac_f32_e32 v4, v113, v41
	v_fmac_f32_e32 v4, v114, v42
	v_fmac_f32_e32 v4, v115, v43
	s_waitcnt lgkmcnt(0)
	v_fmac_f32_e32 v5, v112, v44
	v_fmac_f32_e32 v5, v113, v45
	v_fmac_f32_e32 v5, v114, v46
	v_fmac_f32_e32 v5, v115, v47
	ds_read_b128 v[16:19], v15 offset:336
	ds_read_b128 v[20:23], v15 offset:4432
	ds_read_b128 v[24:27], v15 offset:8528
	ds_read_b128 v[28:31], v15 offset:12624
	ds_read_b128 v[32:35], v15 offset:16720
	ds_read_b128 v[36:39], v15 offset:20816
	ds_read_b128 v[40:43], v15 offset:24912
	ds_read_b128 v[44:47], v15 offset:29008
	s_waitcnt lgkmcnt(7)
	v_fmac_f32_e32 v6, v116, v16
	v_fmac_f32_e32 v6, v117, v17
	v_fmac_f32_e32 v6, v118, v18
	v_fmac_f32_e32 v6, v119, v19
	s_waitcnt lgkmcnt(6)
	v_fmac_f32_e32 v7, v116, v20
	v_fmac_f32_e32 v7, v117, v21
	v_fmac_f32_e32 v7, v118, v22
	v_fmac_f32_e32 v7, v119, v23
	s_waitcnt lgkmcnt(5)
	v_fmac_f32_e32 v8, v116, v24
	v_fmac_f32_e32 v8, v117, v25
	v_fmac_f32_e32 v8, v118, v26
	v_fmac_f32_e32 v8, v119, v27
	s_waitcnt lgkmcnt(4)
	v_fmac_f32_e32 v9, v116, v28
	v_fmac_f32_e32 v9, v117, v29
	v_fmac_f32_e32 v9, v118, v30
	v_fmac_f32_e32 v9, v119, v31
	s_waitcnt lgkmcnt(3)
	v_fmac_f32_e32 v10, v116, v32
	v_fmac_f32_e32 v10, v117, v33
	v_fmac_f32_e32 v10, v118, v34
	v_fmac_f32_e32 v10, v119, v35
	s_waitcnt lgkmcnt(2)
	v_fmac_f32_e32 v11, v116, v36
	v_fmac_f32_e32 v11, v117, v37
	v_fmac_f32_e32 v11, v118, v38
	v_fmac_f32_e32 v11, v119, v39
	s_waitcnt lgkmcnt(1)
	v_fmac_f32_e32 v4, v116, v40
	v_fmac_f32_e32 v4, v117, v41
	v_fmac_f32_e32 v4, v118, v42
	v_fmac_f32_e32 v4, v119, v43
	s_waitcnt lgkmcnt(0)
	v_fmac_f32_e32 v5, v116, v44
	v_fmac_f32_e32 v5, v117, v45
	v_fmac_f32_e32 v5, v118, v46
	v_fmac_f32_e32 v5, v119, v47
	ds_read_b128 v[16:19], v15 offset:352
	ds_read_b128 v[20:23], v15 offset:4448
	ds_read_b128 v[24:27], v15 offset:8544
	ds_read_b128 v[28:31], v15 offset:12640
	ds_read_b128 v[32:35], v15 offset:16736
	ds_read_b128 v[36:39], v15 offset:20832
	ds_read_b128 v[40:43], v15 offset:24928
	ds_read_b128 v[44:47], v15 offset:29024
	s_waitcnt lgkmcnt(7)
	v_fmac_f32_e32 v6, v120, v16
	v_fmac_f32_e32 v6, v121, v17
	v_fmac_f32_e32 v6, v122, v18
	v_fmac_f32_e32 v6, v123, v19
	s_waitcnt lgkmcnt(6)
	v_fmac_f32_e32 v7, v120, v20
	v_fmac_f32_e32 v7, v121, v21
	v_fmac_f32_e32 v7, v122, v22
	v_fmac_f32_e32 v7, v123, v23
	s_waitcnt lgkmcnt(5)
	v_fmac_f32_e32 v8, v120, v24
	v_fmac_f32_e32 v8, v121, v25
	v_fmac_f32_e32 v8, v122, v26
	v_fmac_f32_e32 v8, v123, v27
	s_waitcnt lgkmcnt(4)
	v_fmac_f32_e32 v9, v120, v28
	v_fmac_f32_e32 v9, v121, v29
	v_fmac_f32_e32 v9, v122, v30
	v_fmac_f32_e32 v9, v123, v31
	s_waitcnt lgkmcnt(3)
	v_fmac_f32_e32 v10, v120, v32
	v_fmac_f32_e32 v10, v121, v33
	v_fmac_f32_e32 v10, v122, v34
	v_fmac_f32_e32 v10, v123, v35
	s_waitcnt lgkmcnt(2)
; DI void phase_prologue(const Frame& F) {
;     ...
;         for (int k = 0; k < 128; ++k) { const float wv = wp[(size_t)k * 6144];
; #pragma unroll
;             for (int b = 0; b < 8; ++b) acc[b] += ca[b * D + kq * 128 + k] * wv; }
	v_fmac_f32_e32 v11, v120, v36
	v_fmac_f32_e32 v11, v121, v37
	v_fmac_f32_e32 v11, v122, v38
	v_fmac_f32_e32 v11, v123, v39
	s_waitcnt lgkmcnt(1)
	v_fmac_f32_e32 v4, v120, v40
	v_fmac_f32_e32 v4, v121, v41
	v_fmac_f32_e32 v4, v122, v42
	v_fmac_f32_e32 v4, v123, v43
	s_waitcnt lgkmcnt(0)
	v_fmac_f32_e32 v5, v120, v44
	v_fmac_f32_e32 v5, v121, v45
	v_fmac_f32_e32 v5, v122, v46
	v_fmac_f32_e32 v5, v123, v47
	ds_read_b128 v[16:19], v15 offset:368
	ds_read_b128 v[20:23], v15 offset:4464
	ds_read_b128 v[24:27], v15 offset:8560
	ds_read_b128 v[28:31], v15 offset:12656
	ds_read_b128 v[32:35], v15 offset:16752
	ds_read_b128 v[36:39], v15 offset:20848
	ds_read_b128 v[40:43], v15 offset:24944
	ds_read_b128 v[44:47], v15 offset:29040
	s_waitcnt lgkmcnt(7)
	v_fmac_f32_e32 v6, v124, v16
	v_fmac_f32_e32 v6, v125, v17
	v_fmac_f32_e32 v6, v126, v18
	v_fmac_f32_e32 v6, v127, v19
	s_waitcnt lgkmcnt(6)
	v_fmac_f32_e32 v7, v124, v20
	v_fmac_f32_e32 v7, v125, v21
	v_fmac_f32_e32 v7, v126, v22
	v_fmac_f32_e32 v7, v127, v23
	s_waitcnt lgkmcnt(5)
	v_fmac_f32_e32 v8, v124, v24
	v_fmac_f32_e32 v8, v125, v25
	v_fmac_f32_e32 v8, v126, v26
	v_fmac_f32_e32 v8, v127, v27
	s_waitcnt lgkmcnt(4)
	v_fmac_f32_e32 v9, v124, v28
	v_fmac_f32_e32 v9, v125, v29
	v_fmac_f32_e32 v9, v126, v30
	v_fmac_f32_e32 v9, v127, v31
	s_waitcnt lgkmcnt(3)
	v_fmac_f32_e32 v10, v124, v32
	v_fmac_f32_e32 v10, v125, v33
	v_fmac_f32_e32 v10, v126, v34
	v_fmac_f32_e32 v10, v127, v35
	s_waitcnt lgkmcnt(2)
	v_fmac_f32_e32 v11, v124, v36
	v_fmac_f32_e32 v11, v125, v37
	v_fmac_f32_e32 v11, v126, v38
	v_fmac_f32_e32 v11, v127, v39
	s_waitcnt lgkmcnt(1)
	v_fmac_f32_e32 v4, v124, v40
	v_fmac_f32_e32 v4, v125, v41
	v_fmac_f32_e32 v4, v126, v42
	v_fmac_f32_e32 v4, v127, v43
	s_waitcnt lgkmcnt(0)
	v_fmac_f32_e32 v5, v124, v44
	v_fmac_f32_e32 v5, v125, v45
	v_fmac_f32_e32 v5, v126, v46
	v_fmac_f32_e32 v5, v127, v47
	s_waitcnt vmcnt(16)
	ds_read_b128 v[16:19], v15 offset:384
	ds_read_b128 v[20:23], v15 offset:4480
	ds_read_b128 v[24:27], v15 offset:8576
	ds_read_b128 v[28:31], v15 offset:12672
	ds_read_b128 v[32:35], v15 offset:16768
	ds_read_b128 v[36:39], v15 offset:20864
	ds_read_b128 v[40:43], v15 offset:24960
	ds_read_b128 v[44:47], v15 offset:29056
	s_waitcnt lgkmcnt(7)
	v_fmac_f32_e32 v6, v149, v16
	v_fmac_f32_e32 v6, v150, v17
	v_fmac_f32_e32 v6, v151, v18
	v_fmac_f32_e32 v6, v152, v19
	s_waitcnt lgkmcnt(6)
	v_fmac_f32_e32 v7, v149, v20
	v_fmac_f32_e32 v7, v150, v21
	v_fmac_f32_e32 v7, v151, v22
	v_fmac_f32_e32 v7, v152, v23
	s_waitcnt lgkmcnt(5)
	v_fmac_f32_e32 v8, v149, v24
	v_fmac_f32_e32 v8, v150, v25
	v_fmac_f32_e32 v8, v151, v26
	v_fmac_f32_e32 v8, v152, v27
	s_waitcnt lgkmcnt(4)
	v_fmac_f32_e32 v9, v149, v28
	v_fmac_f32_e32 v9, v150, v29
	v_fmac_f32_e32 v9, v151, v30
	v_fmac_f32_e32 v9, v152, v31
	s_waitcnt lgkmcnt(3)
	v_fmac_f32_e32 v10, v149, v32
	v_fmac_f32_e32 v10, v150, v33
	v_fmac_f32_e32 v10, v151, v34
	v_fmac_f32_e32 v10, v152, v35
	s_waitcnt lgkmcnt(2)
	v_fmac_f32_e32 v11, v149, v36
	v_fmac_f32_e32 v11, v150, v37
	v_fmac_f32_e32 v11, v151, v38
	v_fmac_f32_e32 v11, v152, v39
	s_waitcnt lgkmcnt(1)
	v_fmac_f32_e32 v4, v149, v40
	v_fmac_f32_e32 v4, v150, v41
	v_fmac_f32_e32 v4, v151, v42
	v_fmac_f32_e32 v4, v152, v43
	s_waitcnt lgkmcnt(0)
	v_fmac_f32_e32 v5, v149, v44
	v_fmac_f32_e32 v5, v150, v45
	v_fmac_f32_e32 v5, v151, v46
	v_fmac_f32_e32 v5, v152, v47
	ds_read_b128 v[16:19], v15 offset:400
	ds_read_b128 v[20:23], v15 offset:4496
	ds_read_b128 v[24:27], v15 offset:8592
	ds_read_b128 v[28:31], v15 offset:12688
	ds_read_b128 v[32:35], v15 offset:16784
	ds_read_b128 v[36:39], v15 offset:20880
	ds_read_b128 v[40:43], v15 offset:24976
	ds_read_b128 v[44:47], v15 offset:29072
	s_waitcnt lgkmcnt(7)
	v_fmac_f32_e32 v6, v153, v16
	v_fmac_f32_e32 v6, v154, v17
	v_fmac_f32_e32 v6, v155, v18
	v_fmac_f32_e32 v6, v156, v19
	s_waitcnt lgkmcnt(6)
	v_fmac_f32_e32 v7, v153, v20
	v_fmac_f32_e32 v7, v154, v21
	v_fmac_f32_e32 v7, v155, v22
	v_fmac_f32_e32 v7, v156, v23
	s_waitcnt lgkmcnt(5)
	v_fmac_f32_e32 v8, v153, v24
	v_fmac_f32_e32 v8, v154, v25
	v_fmac_f32_e32 v8, v155, v26
	v_fmac_f32_e32 v8, v156, v27
	s_waitcnt lgkmcnt(4)
	v_fmac_f32_e32 v9, v153, v28
	v_fmac_f32_e32 v9, v154, v29
	v_fmac_f32_e32 v9, v155, v30
	v_fmac_f32_e32 v9, v156, v31
	s_waitcnt lgkmcnt(3)
	v_fmac_f32_e32 v10, v153, v32
	v_fmac_f32_e32 v10, v154, v33
	v_fmac_f32_e32 v10, v155, v34
	v_fmac_f32_e32 v10, v156, v35
	s_waitcnt lgkmcnt(2)
	v_fmac_f32_e32 v11, v153, v36
	v_fmac_f32_e32 v11, v154, v37
	v_fmac_f32_e32 v11, v155, v38
	v_fmac_f32_e32 v11, v156, v39
	s_waitcnt lgkmcnt(1)
	v_fmac_f32_e32 v4, v153, v40
	v_fmac_f32_e32 v4, v154, v41
	v_fmac_f32_e32 v4, v155, v42
	v_fmac_f32_e32 v4, v156, v43
	s_waitcnt lgkmcnt(0)
	v_fmac_f32_e32 v5, v153, v44
	v_fmac_f32_e32 v5, v154, v45
	v_fmac_f32_e32 v5, v155, v46
	v_fmac_f32_e32 v5, v156, v47
	ds_read_b128 v[16:19], v15 offset:416
	ds_read_b128 v[20:23], v15 offset:4512
	ds_read_b128 v[24:27], v15 offset:8608
	ds_read_b128 v[28:31], v15 offset:12704
	ds_read_b128 v[32:35], v15 offset:16800
	ds_read_b128 v[36:39], v15 offset:20896
	ds_read_b128 v[40:43], v15 offset:24992
	ds_read_b128 v[44:47], v15 offset:29088
	s_waitcnt lgkmcnt(7)
	v_fmac_f32_e32 v6, v157, v16
	v_fmac_f32_e32 v6, v158, v17
	v_fmac_f32_e32 v6, v159, v18
	v_fmac_f32_e32 v6, v160, v19
	s_waitcnt lgkmcnt(6)
	v_fmac_f32_e32 v7, v157, v20
	v_fmac_f32_e32 v7, v158, v21
	v_fmac_f32_e32 v7, v159, v22
	v_fmac_f32_e32 v7, v160, v23
	s_waitcnt lgkmcnt(5)
	v_fmac_f32_e32 v8, v157, v24
	v_fmac_f32_e32 v8, v158, v25
	v_fmac_f32_e32 v8, v159, v26
	v_fmac_f32_e32 v8, v160, v27
	s_waitcnt lgkmcnt(4)
; DI void phase_prologue(const Frame& F) {
;     ...
;         for (int k = 0; k < 128; ++k) { const float wv = wp[(size_t)k * 6144];
; #pragma unroll
;             for (int b = 0; b < 8; ++b) acc[b] += ca[b * D + kq * 128 + k] * wv; }
	v_fmac_f32_e32 v9, v157, v28
	v_fmac_f32_e32 v9, v158, v29
	v_fmac_f32_e32 v9, v159, v30
	v_fmac_f32_e32 v9, v160, v31
	s_waitcnt lgkmcnt(3)
	v_fmac_f32_e32 v10, v157, v32
	v_fmac_f32_e32 v10, v158, v33
	v_fmac_f32_e32 v10, v159, v34
	v_fmac_f32_e32 v10, v160, v35
	s_waitcnt lgkmcnt(2)
	v_fmac_f32_e32 v11, v157, v36
	v_fmac_f32_e32 v11, v158, v37
	v_fmac_f32_e32 v11, v159, v38
	v_fmac_f32_e32 v11, v160, v39
	s_waitcnt lgkmcnt(1)
	v_fmac_f32_e32 v4, v157, v40
	v_fmac_f32_e32 v4, v158, v41
	v_fmac_f32_e32 v4, v159, v42
	v_fmac_f32_e32 v4, v160, v43
	s_waitcnt lgkmcnt(0)
	v_fmac_f32_e32 v5, v157, v44
	v_fmac_f32_e32 v5, v158, v45
	v_fmac_f32_e32 v5, v159, v46
	v_fmac_f32_e32 v5, v160, v47
	ds_read_b128 v[16:19], v15 offset:432
	ds_read_b128 v[20:23], v15 offset:4528
	ds_read_b128 v[24:27], v15 offset:8624
	ds_read_b128 v[28:31], v15 offset:12720
	ds_read_b128 v[32:35], v15 offset:16816
	ds_read_b128 v[36:39], v15 offset:20912
	ds_read_b128 v[40:43], v15 offset:25008
	ds_read_b128 v[44:47], v15 offset:29104
	s_waitcnt lgkmcnt(7)
	v_fmac_f32_e32 v6, v161, v16
	v_fmac_f32_e32 v6, v162, v17
	v_fmac_f32_e32 v6, v163, v18
	v_fmac_f32_e32 v6, v164, v19
	s_waitcnt lgkmcnt(6)
	v_fmac_f32_e32 v7, v161, v20
	v_fmac_f32_e32 v7, v162, v21
	v_fmac_f32_e32 v7, v163, v22
	v_fmac_f32_e32 v7, v164, v23
	s_waitcnt lgkmcnt(5)
	v_fmac_f32_e32 v8, v161, v24
	v_fmac_f32_e32 v8, v162, v25
	v_fmac_f32_e32 v8, v163, v26
	v_fmac_f32_e32 v8, v164, v27
	s_waitcnt lgkmcnt(4)
	v_fmac_f32_e32 v9, v161, v28
	v_fmac_f32_e32 v9, v162, v29
	v_fmac_f32_e32 v9, v163, v30
	v_fmac_f32_e32 v9, v164, v31
	s_waitcnt lgkmcnt(3)
	v_fmac_f32_e32 v10, v161, v32
	v_fmac_f32_e32 v10, v162, v33
	v_fmac_f32_e32 v10, v163, v34
	v_fmac_f32_e32 v10, v164, v35
	s_waitcnt lgkmcnt(2)
	v_fmac_f32_e32 v11, v161, v36
	v_fmac_f32_e32 v11, v162, v37
	v_fmac_f32_e32 v11, v163, v38
	v_fmac_f32_e32 v11, v164, v39
	s_waitcnt lgkmcnt(1)
	v_fmac_f32_e32 v4, v161, v40
	v_fmac_f32_e32 v4, v162, v41
	v_fmac_f32_e32 v4, v163, v42
	v_fmac_f32_e32 v4, v164, v43
	s_waitcnt lgkmcnt(0)
	v_fmac_f32_e32 v5, v161, v44
	v_fmac_f32_e32 v5, v162, v45
	v_fmac_f32_e32 v5, v163, v46
	v_fmac_f32_e32 v5, v164, v47
	s_waitcnt vmcnt(0)
	ds_read_b128 v[16:19], v15 offset:448
	ds_read_b128 v[20:23], v15 offset:4544
	ds_read_b128 v[24:27], v15 offset:8640
	ds_read_b128 v[28:31], v15 offset:12736
	ds_read_b128 v[32:35], v15 offset:16832
	ds_read_b128 v[36:39], v15 offset:20928
	ds_read_b128 v[40:43], v15 offset:25024
	ds_read_b128 v[44:47], v15 offset:29120
	s_waitcnt lgkmcnt(7)
	v_fmac_f32_e32 v6, v165, v16
	v_fmac_f32_e32 v6, v166, v17
	v_fmac_f32_e32 v6, v167, v18
	v_fmac_f32_e32 v6, v168, v19
	s_waitcnt lgkmcnt(6)
	v_fmac_f32_e32 v7, v165, v20
	v_fmac_f32_e32 v7, v166, v21
	v_fmac_f32_e32 v7, v167, v22
	v_fmac_f32_e32 v7, v168, v23
	s_waitcnt lgkmcnt(5)
	v_fmac_f32_e32 v8, v165, v24
	v_fmac_f32_e32 v8, v166, v25
	v_fmac_f32_e32 v8, v167, v26
	v_fmac_f32_e32 v8, v168, v27
	s_waitcnt lgkmcnt(4)
	v_fmac_f32_e32 v9, v165, v28
	v_fmac_f32_e32 v9, v166, v29
	v_fmac_f32_e32 v9, v167, v30
	v_fmac_f32_e32 v9, v168, v31
	s_waitcnt lgkmcnt(3)
	v_fmac_f32_e32 v10, v165, v32
	v_fmac_f32_e32 v10, v166, v33
	v_fmac_f32_e32 v10, v167, v34
	v_fmac_f32_e32 v10, v168, v35
	s_waitcnt lgkmcnt(2)
	v_fmac_f32_e32 v11, v165, v36
	v_fmac_f32_e32 v11, v166, v37
	v_fmac_f32_e32 v11, v167, v38
	v_fmac_f32_e32 v11, v168, v39
	s_waitcnt lgkmcnt(1)
	v_fmac_f32_e32 v4, v165, v40
	v_fmac_f32_e32 v4, v166, v41
	v_fmac_f32_e32 v4, v167, v42
	v_fmac_f32_e32 v4, v168, v43
	s_waitcnt lgkmcnt(0)
	v_fmac_f32_e32 v5, v165, v44
	v_fmac_f32_e32 v5, v166, v45
	v_fmac_f32_e32 v5, v167, v46
	v_fmac_f32_e32 v5, v168, v47
	ds_read_b128 v[16:19], v15 offset:464
	ds_read_b128 v[20:23], v15 offset:4560
	ds_read_b128 v[24:27], v15 offset:8656
	ds_read_b128 v[28:31], v15 offset:12752
	ds_read_b128 v[32:35], v15 offset:16848
	ds_read_b128 v[36:39], v15 offset:20944
	ds_read_b128 v[40:43], v15 offset:25040
	ds_read_b128 v[44:47], v15 offset:29136
	s_waitcnt lgkmcnt(7)
	v_fmac_f32_e32 v6, v169, v16
	v_fmac_f32_e32 v6, v170, v17
	v_fmac_f32_e32 v6, v171, v18
	v_fmac_f32_e32 v6, v172, v19
	s_waitcnt lgkmcnt(6)
	v_fmac_f32_e32 v7, v169, v20
	v_fmac_f32_e32 v7, v170, v21
	v_fmac_f32_e32 v7, v171, v22
	v_fmac_f32_e32 v7, v172, v23
	s_waitcnt lgkmcnt(5)
	v_fmac_f32_e32 v8, v169, v24
	v_fmac_f32_e32 v8, v170, v25
	v_fmac_f32_e32 v8, v171, v26
	v_fmac_f32_e32 v8, v172, v27
	s_waitcnt lgkmcnt(4)
	v_fmac_f32_e32 v9, v169, v28
	v_fmac_f32_e32 v9, v170, v29
	v_fmac_f32_e32 v9, v171, v30
	v_fmac_f32_e32 v9, v172, v31
	s_waitcnt lgkmcnt(3)
	v_fmac_f32_e32 v10, v169, v32
	v_fmac_f32_e32 v10, v170, v33
	v_fmac_f32_e32 v10, v171, v34
	v_fmac_f32_e32 v10, v172, v35
	s_waitcnt lgkmcnt(2)
; DI void phase_prologue(const Frame& F) {
;     ...
;         for (int k = 0; k < 128; ++k) { const float wv = wp[(size_t)k * 6144];
; #pragma unroll
;             for (int b = 0; b < 8; ++b) acc[b] += ca[b * D + kq * 128 + k] * wv; }
; #pragma unroll
;         for (int b = 0; b < 8; ++b) red[(kq * 8 + b) * 64 + F.lane] = acc[b];
;         __syncthreads();
;         { const int b = F.wave; float s = F.ap->in[3][(size_t)l * 6144 + n];
; #pragma unroll
;           for (int q = 0; q < 8; ++q) s += red[(q * 8 + b) * 64 + F.lane];
;           ((float*)(ws + WS_MOD))[((size_t)l * NB + b) * 6144 + n] = s; }
;         __syncthreads();
;     }
	v_fmac_f32_e32 v11, v169, v36
	v_fmac_f32_e32 v11, v170, v37
	v_fmac_f32_e32 v11, v171, v38
	v_fmac_f32_e32 v11, v172, v39
	s_waitcnt lgkmcnt(1)
	v_fmac_f32_e32 v4, v169, v40
	v_fmac_f32_e32 v4, v170, v41
	v_fmac_f32_e32 v4, v171, v42
	v_fmac_f32_e32 v4, v172, v43
	s_waitcnt lgkmcnt(0)
	v_fmac_f32_e32 v5, v169, v44
	v_fmac_f32_e32 v5, v170, v45
	v_fmac_f32_e32 v5, v171, v46
	v_fmac_f32_e32 v5, v172, v47
	ds_read_b128 v[16:19], v15 offset:480
	ds_read_b128 v[20:23], v15 offset:4576
	ds_read_b128 v[24:27], v15 offset:8672
	ds_read_b128 v[28:31], v15 offset:12768
	ds_read_b128 v[32:35], v15 offset:16864
	ds_read_b128 v[36:39], v15 offset:20960
	ds_read_b128 v[40:43], v15 offset:25056
	ds_read_b128 v[44:47], v15 offset:29152
	s_waitcnt lgkmcnt(7)
	v_fmac_f32_e32 v6, v173, v16
	v_fmac_f32_e32 v6, v174, v17
	v_fmac_f32_e32 v6, v175, v18
	v_fmac_f32_e32 v6, v176, v19
	s_waitcnt lgkmcnt(6)
	v_fmac_f32_e32 v7, v173, v20
	v_fmac_f32_e32 v7, v174, v21
	v_fmac_f32_e32 v7, v175, v22
	v_fmac_f32_e32 v7, v176, v23
	s_waitcnt lgkmcnt(5)
	v_fmac_f32_e32 v8, v173, v24
	v_fmac_f32_e32 v8, v174, v25
	v_fmac_f32_e32 v8, v175, v26
	v_fmac_f32_e32 v8, v176, v27
	s_waitcnt lgkmcnt(4)
	v_fmac_f32_e32 v9, v173, v28
	v_fmac_f32_e32 v9, v174, v29
	v_fmac_f32_e32 v9, v175, v30
	v_fmac_f32_e32 v9, v176, v31
	s_waitcnt lgkmcnt(3)
	v_fmac_f32_e32 v10, v173, v32
	v_fmac_f32_e32 v10, v174, v33
	v_fmac_f32_e32 v10, v175, v34
	v_fmac_f32_e32 v10, v176, v35
	s_waitcnt lgkmcnt(2)
	v_fmac_f32_e32 v11, v173, v36
	v_fmac_f32_e32 v11, v174, v37
	v_fmac_f32_e32 v11, v175, v38
	v_fmac_f32_e32 v11, v176, v39
	s_waitcnt lgkmcnt(1)
	v_fmac_f32_e32 v4, v173, v40
	v_fmac_f32_e32 v4, v174, v41
	v_fmac_f32_e32 v4, v175, v42
	v_fmac_f32_e32 v4, v176, v43
	s_waitcnt lgkmcnt(0)
	v_fmac_f32_e32 v5, v173, v44
	v_fmac_f32_e32 v5, v174, v45
	v_fmac_f32_e32 v5, v175, v46
	v_fmac_f32_e32 v5, v176, v47
	ds_read_b128 v[16:19], v15 offset:496
	ds_read_b128 v[20:23], v15 offset:4592
	ds_read_b128 v[24:27], v15 offset:8688
	ds_read_b128 v[28:31], v15 offset:12784
	ds_read_b128 v[32:35], v15 offset:16880
	ds_read_b128 v[36:39], v15 offset:20976
	ds_read_b128 v[40:43], v15 offset:25072
	ds_read_b128 v[44:47], v15 offset:29168
	s_waitcnt lgkmcnt(7)
	v_fmac_f32_e32 v6, v177, v16
	v_fmac_f32_e32 v6, v178, v17
	v_fmac_f32_e32 v6, v179, v18
	v_fmac_f32_e32 v6, v180, v19
	s_waitcnt lgkmcnt(6)
	v_fmac_f32_e32 v7, v177, v20
	v_fmac_f32_e32 v7, v178, v21
	v_fmac_f32_e32 v7, v179, v22
	v_fmac_f32_e32 v7, v180, v23
	s_waitcnt lgkmcnt(5)
	v_fmac_f32_e32 v8, v177, v24
	v_fmac_f32_e32 v8, v178, v25
	v_fmac_f32_e32 v8, v179, v26
	v_fmac_f32_e32 v8, v180, v27
	s_waitcnt lgkmcnt(4)
	v_fmac_f32_e32 v9, v177, v28
	v_fmac_f32_e32 v9, v178, v29
	v_fmac_f32_e32 v9, v179, v30
	v_fmac_f32_e32 v9, v180, v31
	s_waitcnt lgkmcnt(3)
	v_fmac_f32_e32 v10, v177, v32
	v_fmac_f32_e32 v10, v178, v33
	v_fmac_f32_e32 v10, v179, v34
	v_fmac_f32_e32 v10, v180, v35
	s_waitcnt lgkmcnt(2)
	v_fmac_f32_e32 v11, v177, v36
	v_fmac_f32_e32 v11, v178, v37
	v_fmac_f32_e32 v11, v179, v38
	v_fmac_f32_e32 v11, v180, v39
	s_waitcnt lgkmcnt(1)
	v_fmac_f32_e32 v4, v177, v40
	v_fmac_f32_e32 v4, v178, v41
	v_fmac_f32_e32 v4, v179, v42
	v_fmac_f32_e32 v4, v180, v43
	s_waitcnt lgkmcnt(0)
	v_fmac_f32_e32 v5, v177, v44
	v_fmac_f32_e32 v5, v178, v45
	v_fmac_f32_e32 v5, v179, v46
	v_fmac_f32_e32 v5, v180, v47
	s_mul_i32 s14, s4, 0x6000
	s_mul_hi_i32 s13, s4, 0x6000
	s_add_u32 s14, s38, s14
	s_addc_u32 s15, s39, s13
	v_lshlrev_b64 v[0:1], 2, v[0:1]
	v_lshl_add_u64 v[2:3], s[14:15], 0, v[0:1]
	ds_write2st64_b32 v12, v6, v7 offset0:128 offset1:129
	ds_write2st64_b32 v12, v8, v9 offset0:130 offset1:131
	ds_write2st64_b32 v12, v10, v11 offset0:132 offset1:133
	ds_write2st64_b32 v12, v4, v5 offset0:134 offset1:135
	s_waitcnt lgkmcnt(0)
	s_barrier
	global_load_dword v10, v[2:3], off
	ds_read2st64_b32 v[2:3], v13 offset0:128 offset1:136
	ds_read2st64_b32 v[4:5], v13 offset0:144 offset1:152
	ds_read2st64_b32 v[6:7], v13 offset0:160 offset1:168
	ds_read2st64_b32 v[8:9], v13 offset0:176 offset1:184
	s_lshl_b64 s[4:5], s[4:5], 3
	s_add_u32 s4, s4, s11
	s_addc_u32 s5, s5, s12
	s_mul_hi_u32 s13, s4, 0x6000
	s_mulk_i32 s5, 0x6000
	s_mulk_i32 s4, 0x6000
	s_add_i32 s13, s13, s5
	s_add_u32 s4, s2, s4
	s_addc_u32 s5, s6, s13
	s_add_i32 s3, s3, s10
	v_lshl_add_u64 v[0:1], s[4:5], 0, v[0:1]
	s_cmpk_gt_i32 s3, 0x17f
	s_waitcnt vmcnt(0) lgkmcnt(3)
	v_add_f32_e32 v2, v10, v2
	v_add_f32_e32 v2, v2, v3
	s_waitcnt lgkmcnt(2)
	v_add_f32_e32 v2, v2, v4
	v_add_f32_e32 v2, v2, v5
	s_waitcnt lgkmcnt(1)
	v_add_f32_e32 v2, v2, v6
	v_add_f32_e32 v2, v2, v7
	s_waitcnt lgkmcnt(0)
	v_add_f32_e32 v2, v2, v8
	v_add_f32_e32 v2, v2, v9
	global_store_dword v[0:1], v2, off
	s_barrier
	s_cbranch_scc0 .LBB0_51

; #define LAS __attribute__((address_space(3)))
; DI unsigned cvt2(float lo, float hi) { return __builtin_bit_cast(unsigned, __builtin_convertvector((f32x2){lo, hi}, bfv2)); }
; DI void phase_chain(const Frame& F) {
;     ...
;             for (int jj = 0; jj < NSUB; ++jj) {
;                 __builtin_amdgcn_s_barrier(); asm volatile("" ::: "memory");
;                 const LAS unsigned char* st = ring + cur * CH_STB;
;                 bf16x8 sb[4]; sb[0] = pack8(S0, 0); sb[1] = pack8(S0, 1); sb[2] = pack8(S1, 0); sb[3] = pack8(S1, 1);
;                 const bf16x8 vt = *(const LAS bf16x8*)(st + 12800 + r * 32 + h * 16), wh = *(const LAS bf16x8*)(st + 12288 + rs * 32 + h * 16);
;                 const bf16x8 kh0 = *(const LAS bf16x8*)(st + 8192 + r * 32 + h * 16), kh1 = *(const LAS bf16x8*)(st + 8192 + (32 + r) * 32 + h * 16);
;                 f32x16 Y, N0, N1;
; #pragma unroll
;                 for (int i = 0; i < 16; ++i) { Y[i] = 0.f; N0[i] = 0.f; N1[i] = 0.f; }
;                 Y = __builtin_amdgcn_mfma_f32_32x32x16_bf16(wh, vt, Y, 0, 0, 0);
;                 N0 = __builtin_amdgcn_mfma_f32_32x32x16_bf16(kh0, vt, N0, 0, 0, 0);
;                 N1 = __builtin_amdgcn_mfma_f32_32x32x16_bf16(kh1, vt, N1, 0, 0, 0);
; #pragma unroll
;                 for (int ks = 0; ks < 4; ++ks) { const int c0 = ((4 * ks + h) ^ rs) * 8, c1 = ((4 * ks + h + 2) ^ rs) * 8;
;                     Y = __builtin_amdgcn_mfma_f32_32x32x16_bf16(cat8(st + 10240 + rs * 128 + c0, st + 10240 + rs * 128 + c1), sb[ks], Y, 0, 0, 0);
;                     N0 = __builtin_amdgcn_mfma_f32_32x32x16_bf16(cat8(st + r * 128 + c0, st + r * 128 + c1), sb[ks], N0, 0, 0, 0);
;                     N1 = __builtin_amdgcn_mfma_f32_32x32x16_bf16(cat8(st + (32 + r) * 128 + c0, st + (32 + r) * 128 + c1), sb[ks], N1, 0, 0, 0); }
;                 S0 = N0; S1 = N1;
; #pragma unroll
;                 for (int q = 0; q < 8; q += 1) { const int t = (q & 3) + 8 * (q >> 2) + 4 * h; *(LAS bf16_t*)(ybuf + (t * 32 + r) * 2) = (bf16_t)(cvt2(Y[q], 0.f) & 0xffffu); }
;                 { const u32x4 w = *(const LAS u32x4*)(ybuf + F.lane * 16); const int t = F.lane >> 2, step = 16 * jj + t, tt = d ? (SEQ - 1 - step) : step;
;                   *(u32x4*)(YD + ((size_t)d * T + (size_t)b * SEQ + tt) * 512 + hd * 64 + 32 * rb + 8 * (F.lane & 3)) = w; }
;                 cur = cur == CH_NST - 1 ? 0 : cur + 1;
;             }
.LBB0_753:
	s_mov_b64 s[4:5], -1
	s_and_b64 vcc, exec, s[42:43]
	s_cbranch_vccz .LBB0_765
	s_ashr_i32 s50, s6, 1
	s_and_b32 s10, s6, 1
	s_andn2_b64 vcc, exec, s[44:45]
	s_cbranch_vccnz .LBB0_758
	s_ashr_i32 s12, s6, 5
	s_and_b32 s2, s50, 1
	s_cmp_eq_u32 s2, 0
	s_cselect_b64 vcc, -1, 0
	s_ashr_i32 s13, s12, 31
	s_lshl_b32 s2, s2, 15
	s_lshl_b64 s[12:13], s[12:13], 12
	s_add_u32 s52, s12, s2
	s_addc_u32 s53, s13, 0
	s_lshl_b32 s2, s6, 5
	s_and_b32 s2, s2, 0x380
	s_add_u32 s2, s19, s2
	s_addc_u32 s4, s22, 0
	s_lshl_b32 s12, s10, 6
	s_add_u32 s12, s2, s12
	s_addc_u32 s13, s4, 0
	v_mov_b32_e32 v16, 0
	s_mov_b32 s5, 0
	v_lshl_add_u64 v[74:75], s[12:13], 0, v[192:193]
	s_movk_i32 s4, 0xfff
	v_mov_b32_e32 v101, v91
	v_mov_b32_e32 v17, v16
	v_mov_b32_e32 v18, v16
	v_mov_b32_e32 v19, v16
	v_mov_b32_e32 v20, v16
	v_mov_b32_e32 v21, v16
	v_mov_b32_e32 v22, v16
	v_mov_b32_e32 v23, v16
	v_mov_b32_e32 v24, v16
	v_mov_b32_e32 v25, v16
	v_mov_b32_e32 v26, v16
	v_mov_b32_e32 v27, v16
	v_mov_b32_e32 v28, v16
	v_mov_b32_e32 v29, v16
	v_mov_b32_e32 v30, v16
	v_mov_b32_e32 v31, v16
	v_mov_b32_e32 v0, v16
	v_mov_b32_e32 v1, v16
	v_mov_b32_e32 v2, v16
	v_mov_b32_e32 v3, v16
	v_mov_b32_e32 v4, v16
	v_mov_b32_e32 v5, v16
	v_mov_b32_e32 v6, v16
	v_mov_b32_e32 v7, v16
	v_mov_b32_e32 v8, v16
	v_mov_b32_e32 v9, v16
	v_mov_b32_e32 v10, v16
	v_mov_b32_e32 v11, v16
	v_mov_b32_e32 v12, v16
	v_mov_b32_e32 v13, v16
	v_mov_b32_e32 v14, v16
	v_mov_b32_e32 v15, v16
	s_mul_i32 s2, s5, 0x3800
	v_add3_u32 v126, s2, v78, v77
	v_add3_u32 v127, s2, v76, v77
	v_add3_u32 v128, s2, v79, v77
	v_add_u32_e32 v129, s2, v80
	v_add_u32_e32 v130, s2, v81
	v_add_u32_e32 v131, s2, v82
	v_add_u32_e32 v132, v129, v83
	v_add_u32_e32 v212, v129, v84
	v_add_u32_e32 v213, v130, v83
	v_add_u32_e32 v214, v130, v84
.LBB0_756:
	s_barrier
	ds_read_b128 v[134:137], v126 offset:12288
	ds_read_b128 v[138:141], v127 offset:12800
	ds_read_b128 v[142:145], v127 offset:8192
	ds_read_b128 v[146:149], v128 offset:8192
	ds_read_b64 v[150:151], v132 offset:10240
	ds_read_b64 v[152:153], v212 offset:10240
	v_cvt_pk_bf16_f32 v102, v16, v17
	v_cvt_pk_bf16_f32 v103, v18, v19
	v_cvt_pk_bf16_f32 v104, v20, v21
	v_cvt_pk_bf16_f32 v105, v22, v23
	v_cvt_pk_bf16_f32 v106, v24, v25
	v_cvt_pk_bf16_f32 v107, v26, v27
	v_cvt_pk_bf16_f32 v108, v28, v29
	v_cvt_pk_bf16_f32 v109, v30, v31
	v_cvt_pk_bf16_f32 v52, v0, v1
	v_cvt_pk_bf16_f32 v53, v2, v3
	v_cvt_pk_bf16_f32 v54, v4, v5
	v_cvt_pk_bf16_f32 v55, v6, v7
	v_cvt_pk_bf16_f32 v48, v8, v9
	v_cvt_pk_bf16_f32 v49, v10, v11
	v_cvt_pk_bf16_f32 v50, v12, v13
	v_cvt_pk_bf16_f32 v51, v14, v15
	s_waitcnt lgkmcnt(4)
	s_cmpk_eq_i32 s4, 0xfff
	s_cbranch_scc1 .Lchain_nostore
	global_store_dwordx4 v[210:211], v[206:209], off
.Lchain_nostore:
	v_mfma_f32_32x32x16_bf16 v[32:47], v[134:137], v[138:141], 0
	ds_read_b64 v[154:155], v213
	ds_read_b64 v[156:157], v214
	v_add_u32_e32 v215, v131, v83
	v_add_u32_e32 v216, v131, v84
	ds_read_b64 v[158:159], v215
	ds_read_b64 v[160:161], v216
	v_add_u32_e32 v215, v129, v85
	v_add_u32_e32 v216, v129, v86
	ds_read_b64 v[162:163], v215 offset:10240
	ds_read_b64 v[164:165], v216 offset:10240
	s_waitcnt lgkmcnt(9)
	v_mfma_f32_32x32x16_bf16 v[16:31], v[142:145], v[138:141], 0
	v_add_u32_e32 v215, v130, v85
	v_add_u32_e32 v216, v130, v86
	ds_read_b64 v[166:167], v215
	ds_read_b64 v[168:169], v216
	s_waitcnt lgkmcnt(10)
	v_mfma_f32_32x32x16_bf16 v[0:15], v[146:149], v[138:141], 0
	v_add_u32_e32 v215, v131, v85
	v_add_u32_e32 v216, v131, v86
	ds_read_b64 v[170:171], v215
	ds_read_b64 v[172:173], v216
	s_waitcnt lgkmcnt(10)
	v_mfma_f32_32x32x16_bf16 v[32:47], v[150:153], v[102:105], v[32:47]
	v_add_u32_e32 v215, v129, v87
	v_add_u32_e32 v216, v129, v88
	ds_read_b64 v[174:175], v215 offset:10240
	ds_read_b64 v[176:177], v216 offset:10240
	s_waitcnt lgkmcnt(10)
	v_mfma_f32_32x32x16_bf16 v[16:31], v[154:157], v[102:105], v[16:31]
	v_add_u32_e32 v215, v130, v87
	v_add_u32_e32 v216, v130, v88
	ds_read_b64 v[178:179], v215
	ds_read_b64 v[180:181], v216
	s_waitcnt lgkmcnt(10)
	v_mfma_f32_32x32x16_bf16 v[0:15], v[158:161], v[102:105], v[0:15]
	v_add_u32_e32 v215, v131, v87
	v_add_u32_e32 v216, v131, v88
	ds_read_b64 v[182:183], v215
	ds_read_b64 v[184:185], v216
	s_waitcnt lgkmcnt(10)
	v_mfma_f32_32x32x16_bf16 v[32:47], v[162:165], v[106:109], v[32:47]
	v_add_u32_e32 v215, v129, v89
	v_add_u32_e32 v216, v129, v90
	ds_read_b64 v[194:195], v215 offset:10240
	ds_read_b64 v[196:197], v216 offset:10240
	s_waitcnt lgkmcnt(10)
	v_mfma_f32_32x32x16_bf16 v[16:31], v[166:169], v[106:109], v[16:31]
	v_add_u32_e32 v215, v130, v89
	v_add_u32_e32 v216, v130, v90
	ds_read_b64 v[198:199], v215
	ds_read_b64 v[200:201], v216
	s_waitcnt lgkmcnt(10)
	v_mfma_f32_32x32x16_bf16 v[0:15], v[170:173], v[106:109], v[0:15]
	v_add_u32_e32 v215, v131, v89
	v_add_u32_e32 v216, v131, v90
	ds_read_b64 v[202:203], v215
	ds_read_b64 v[204:205], v216
	s_waitcnt lgkmcnt(10)
	v_mfma_f32_32x32x16_bf16 v[32:47], v[174:177], v[52:55], v[32:47]
	s_waitcnt lgkmcnt(8)
	v_mfma_f32_32x32x16_bf16 v[16:31], v[178:181], v[52:55], v[16:31]
	s_waitcnt lgkmcnt(6)
	v_mfma_f32_32x32x16_bf16 v[0:15], v[182:185], v[52:55], v[0:15]
	s_waitcnt lgkmcnt(4)
	v_mfma_f32_32x32x16_bf16 v[32:47], v[194:197], v[48:51], v[32:47]
	s_waitcnt lgkmcnt(2)
	v_mfma_f32_32x32x16_bf16 v[16:31], v[198:201], v[48:51], v[16:31]
	s_waitcnt lgkmcnt(0)
	v_mfma_f32_32x32x16_bf16 v[0:15], v[202:205], v[48:51], v[0:15]
	s_add_i32 s2, s5, 1
	s_cmp_lg_u32 s5, 5
	s_cselect_b32 s5, s2, 0
	s_mul_i32 s2, s5, 0x3800
	v_add3_u32 v126, s2, v78, v77
	v_add3_u32 v127, s2, v76, v77
	v_add3_u32 v128, s2, v79, v77
	v_add_u32_e32 v129, s2, v80
	v_add_u32_e32 v130, s2, v81
	v_add_u32_e32 v131, s2, v82
	v_add_u32_e32 v132, v129, v83
	v_add_u32_e32 v212, v129, v84
	v_add_u32_e32 v213, v130, v83
	v_add_u32_e32 v214, v130, v84
	v_add_u32_e32 v217, s4, v92
	s_add_i32 s4, s4, -16
	v_cndmask_b32_e32 v210, v217, v101, vcc
	v_ashrrev_i32_e32 v211, 31, v210
	v_lshl_add_u64 v[210:211], s[52:53], 0, v[210:211]
	v_add_u32_e32 v101, 16, v101
	v_lshlrev_b64 v[210:211], 10, v[210:211]
	v_lshl_add_u64 v[210:211], v[74:75], 0, v[210:211]
	v_add_u32_e32 v217, 0x15000, v56
	v_cvt_pk_bf16_f32 v32, v32, s0
	v_cvt_pk_bf16_f32 v33, v33, s0
	v_cvt_pk_bf16_f32 v34, v34, s0
	v_cvt_pk_bf16_f32 v35, v35, s0
	v_cvt_pk_bf16_f32 v36, v36, s0
	v_cvt_pk_bf16_f32 v37, v37, s0
	v_cvt_pk_bf16_f32 v38, v38, s0
	v_cvt_pk_bf16_f32 v39, v39, s0
	ds_write_b16 v93, v32
	ds_write_b16 v94, v33
	ds_write_b16 v95, v34
	ds_write_b16 v96, v35
	ds_write_b16 v97, v36
	ds_write_b16 v98, v37
	ds_write_b16 v99, v38
	ds_write_b16 v100, v39
	ds_read_b128 v[206:209], v217
	s_cmp_eq_u32 s4, -1
	s_cbranch_scc0 .LBB0_756
	s_waitcnt lgkmcnt(0)
	global_store_dwordx4 v[210:211], v[206:209], off
	s_waitcnt vmcnt(0)
	s_waitcnt lgkmcnt(0)
	s_mov_b64 s[4:5], 0
	s_barrier

; DI float kf(float c) { asm volatile("" : "+v"(c)); return c; }
; DI unsigned pk_fp8x4(float a, float b, float c, float d) { int p = 0; p = __builtin_amdgcn_cvt_pk_fp8_f32(a, b, p, false); p = __builtin_amdgcn_cvt_pk_fp8_f32(c, d, p, true); return (unsigned)p; }
;     DI void operator()(const f32x4 (&acc)[2][2][4][2], const Unit& u, int wr, int wc, int fr, int fq) const {
;         const int row0 = u.pm * BM + wr * 64 + fr + (fq & 1) * 16; const int col0 = u.pn * HALF + wc * 32 + 8 * (fq & ~1); const float c7 = kf(7.f);
; #pragma unroll
;         for (int ai = 0; ai < 2; ++ai)
; #pragma unroll
;             for (int mp = 0; mp < 2; ++mp) { unsigned char* rowp = O + (size_t)(row0 + ai * HALF + mp * 32) * ldc + col0;
;                 u32x2 w[2];
; #pragma unroll
;                 for (int mm = 0; mm < 2; ++mm) { const int m = 2 * mp + mm; float o[8];
; #pragma unroll
;                     for (int n = 0; n < 2; ++n) { const f32x4 g = acc[ai][0][m][n], l = acc[ai][1][m][n];
; #pragma unroll
;                         for (int jp = 0; jp < 2; ++jp) {
;                             const f32x2 xg = __builtin_elementwise_min((f32x2){g[2 * jp], g[2 * jp + 1]}, (f32x2){c7, c7});
;                             const f32x2 xl = __builtin_elementwise_min(__builtin_elementwise_max((f32x2){l[2 * jp], l[2 * jp + 1]}, (f32x2){-c7, -c7}), (f32x2){c7, c7});
;                             const f32x2 z = xg * (-1.702f * 1.44269504f); f32x2 e; e.x = __builtin_amdgcn_exp2f(z.x); e.y = __builtin_amdgcn_exp2f(z.y);
;                             const f32x2 dn = e + 1.f; f32x2 rc; rc.x = __builtin_amdgcn_rcpf(dn.x); rc.y = __builtin_amdgcn_rcpf(dn.y);
;                             const f32x2 r2 = (xg * rc) * (xl + 1.f); o[n * 4 + 2 * jp] = r2.x; o[n * 4 + 2 * jp + 1] = r2.y; } }
;                     w[mm].x = pk_fp8x4(o[0], o[1], o[2], o[3]); w[mm].y = pk_fp8x4(o[4], o[5], o[6], o[7]); }
;                 const u32x2 sx = __builtin_amdgcn_permlane16_swap(w[0].x, w[1].x, false, false), sy = __builtin_amdgcn_permlane16_swap(w[0].y, w[1].y, false, false);
;                 *(u32x4*)rowp = (u32x4){sx.x, sy.x, sx.y, sy.y}; }
.LBB0_1192:
	s_lshl_b32 s2, s82, 8
	v_mbcnt_lo_u32_b32 v0, -1, 0
	v_mbcnt_hi_u32_b32 v0, -1, v0
	s_add_i32 s2, s2, s90
	v_and_or_b32 v4, v0, 31, s2
	s_lshl_b32 s2, s10, 7
	v_ashrrev_i32_e32 v0, 1, v0
	s_or_b32 s2, s2, s72
	v_and_b32_e32 v0, -16, v0
	v_mov_b32_e32 v7, 0x40e00000
	v_ashrrev_i32_e32 v5, 31, v4
	v_add_u32_e32 v2, s2, v0
	v_lshlrev_b64 v[0:1], 10, v[4:5]
	v_max_f32_e32 v6, v7, v7
	v_min_f32_e32 v9, v189, v6
	v_min_f32_e32 v8, v188, v6
	v_pk_mul_f32 v[10:11], v[8:9], s[84:85] op_sel_hi:[1,0]
	v_max_f32_e64 v7, -v7, -v7
	v_exp_f32_e32 v10, v10
	v_exp_f32_e32 v11, v11
	s_nop 0
	v_pk_add_f32 v[10:11], v[10:11], 1.0 op_sel_hi:[1,0]
	v_rcp_f32_e32 v10, v10
	v_rcp_f32_e32 v11, v11
	v_med3_f32 v13, v185, v7, v6
	v_med3_f32 v12, v184, v7, v6
	v_pk_mul_f32 v[8:9], v[8:9], v[10:11]
	v_pk_add_f32 v[10:11], v[12:13], 1.0 op_sel_hi:[1,0]
	v_pk_mul_f32 v[10:11], v[10:11], v[8:9]
	v_min_f32_e32 v9, v191, v6
	v_min_f32_e32 v8, v190, v6
	v_pk_mul_f32 v[12:13], v[8:9], s[84:85] op_sel_hi:[1,0]
	v_exp_f32_e32 v12, v12
	v_exp_f32_e32 v13, v13
	v_med3_f32 v15, v187, v7, v6
	v_pk_add_f32 v[12:13], v[12:13], 1.0 op_sel_hi:[1,0]
	v_med3_f32 v14, v186, v7, v6
	v_rcp_f32_e32 v12, v12
	v_rcp_f32_e32 v13, v13
	s_nop 0
	v_pk_mul_f32 v[8:9], v[8:9], v[12:13]
	v_pk_add_f32 v[12:13], v[14:15], 1.0 op_sel_hi:[1,0]
	v_med3_f32 v17, v177, v7, v6
	v_pk_mul_f32 v[12:13], v[12:13], v[8:9]
	v_min_f32_e32 v9, v181, v6
	v_min_f32_e32 v8, v180, v6
	v_pk_mul_f32 v[14:15], v[8:9], s[84:85] op_sel_hi:[1,0]
	v_exp_f32_e32 v14, v14
	v_exp_f32_e32 v15, v15
	v_med3_f32 v16, v176, v7, v6
	v_pk_add_f32 v[14:15], v[14:15], 1.0 op_sel_hi:[1,0]
	v_rcp_f32_e32 v14, v14
	v_rcp_f32_e32 v15, v15
	v_med3_f32 v19, v179, v7, v6
	v_pk_mul_f32 v[8:9], v[8:9], v[14:15]
	v_pk_add_f32 v[14:15], v[16:17], 1.0 op_sel_hi:[1,0]
	v_pk_mul_f32 v[14:15], v[14:15], v[8:9]
	v_min_f32_e32 v9, v183, v6
	v_min_f32_e32 v8, v182, v6
	v_pk_mul_f32 v[16:17], v[8:9], s[84:85] op_sel_hi:[1,0]
	v_exp_f32_e32 v16, v16
	v_exp_f32_e32 v17, v17
	v_med3_f32 v18, v178, v7, v6
	v_pk_add_f32 v[16:17], v[16:17], 1.0 op_sel_hi:[1,0]
	v_med3_f32 v21, v163, v7, v6
	v_rcp_f32_e32 v16, v16
	v_rcp_f32_e32 v17, v17
	v_ashrrev_i32_e32 v3, 31, v2
	v_lshl_add_u64 v[0:1], s[46:47], 0, v[0:1]
	v_lshl_add_u64 v[0:1], v[0:1], 0, v[2:3]
	v_pk_mul_f32 v[16:17], v[8:9], v[16:17]
	v_mov_b32_e32 v9, v193
	v_cvt_pk_fp8_f32 v9, v14, v15
	v_mov_b32_e32 v8, v193
	v_cvt_pk_fp8_f32 v8, v10, v11
	v_pk_add_f32 v[10:11], v[18:19], 1.0 op_sel_hi:[1,0]
	v_pk_mul_f32 v[10:11], v[10:11], v[16:17]
	v_cvt_pk_fp8_f32 v8, v12, v13 op_sel:[0,0,1]
	v_cvt_pk_fp8_f32 v9, v10, v11 op_sel:[0,0,1]
	v_min_f32_e32 v11, v173, v6
	v_min_f32_e32 v10, v172, v6
	v_pk_mul_f32 v[12:13], v[10:11], s[84:85] op_sel_hi:[1,0]
	v_exp_f32_e32 v12, v12
	v_exp_f32_e32 v13, v13
	v_med3_f32 v15, v169, v7, v6
	v_pk_add_f32 v[12:13], v[12:13], 1.0 op_sel_hi:[1,0]
	v_med3_f32 v14, v168, v7, v6
	v_rcp_f32_e32 v12, v12
	v_rcp_f32_e32 v13, v13
	s_nop 0
	v_pk_mul_f32 v[10:11], v[10:11], v[12:13]
	v_pk_add_f32 v[12:13], v[14:15], 1.0 op_sel_hi:[1,0]
	v_med3_f32 v17, v171, v7, v6
	v_pk_mul_f32 v[12:13], v[12:13], v[10:11]
	v_min_f32_e32 v11, v175, v6
	v_min_f32_e32 v10, v174, v6
	v_pk_mul_f32 v[14:15], v[10:11], s[84:85] op_sel_hi:[1,0]
	v_exp_f32_e32 v14, v14
	v_exp_f32_e32 v15, v15
	v_med3_f32 v16, v170, v7, v6
	v_pk_add_f32 v[14:15], v[14:15], 1.0 op_sel_hi:[1,0]
	v_rcp_f32_e32 v14, v14
	v_rcp_f32_e32 v15, v15
	v_med3_f32 v19, v161, v7, v6
	v_or_b32_e32 v4, 32, v4
	v_pk_mul_f32 v[10:11], v[10:11], v[14:15]
	v_pk_add_f32 v[14:15], v[16:17], 1.0 op_sel_hi:[1,0]
	s_mov_b32 s2, 0x20000
	v_pk_mul_f32 v[14:15], v[14:15], v[10:11]
	v_min_f32_e32 v11, v165, v6
	v_min_f32_e32 v10, v164, v6
	v_pk_mul_f32 v[16:17], v[10:11], s[84:85] op_sel_hi:[1,0]
	v_exp_f32_e32 v16, v16
	v_exp_f32_e32 v17, v17
	v_med3_f32 v18, v160, v7, v6
	v_pk_add_f32 v[16:17], v[16:17], 1.0 op_sel_hi:[1,0]
	s_mov_b64 s[4:5], -1
	v_rcp_f32_e32 v16, v16
	v_rcp_f32_e32 v17, v17
	s_nop 0
	v_pk_mul_f32 v[10:11], v[10:11], v[16:17]
	v_pk_add_f32 v[16:17], v[18:19], 1.0 op_sel_hi:[1,0]
	s_nop 0
	v_pk_mul_f32 v[16:17], v[16:17], v[10:11]
	v_min_f32_e32 v11, v167, v6
	v_min_f32_e32 v10, v166, v6
	v_pk_mul_f32 v[18:19], v[10:11], s[84:85] op_sel_hi:[1,0]
	v_exp_f32_e32 v18, v18
	v_exp_f32_e32 v19, v19
	v_med3_f32 v20, v162, v7, v6
	v_ashrrev_i32_e32 v5, 31, v4
	v_pk_add_f32 v[18:19], v[18:19], 1.0 op_sel_hi:[1,0]
	v_lshlrev_b64 v[4:5], 10, v[4:5]
	v_rcp_f32_e32 v18, v18
	v_rcp_f32_e32 v19, v19
	v_lshl_add_u64 v[4:5], s[46:47], 0, v[4:5]
	v_lshl_add_u64 v[2:3], v[4:5], 0, v[2:3]
	v_pk_mul_f32 v[18:19], v[10:11], v[18:19]
	v_mov_b32_e32 v10, v193
	v_mov_b32_e32 v11, v193
	v_cvt_pk_fp8_f32 v10, v12, v13
	v_cvt_pk_fp8_f32 v11, v16, v17
	v_pk_add_f32 v[12:13], v[20:21], 1.0 op_sel_hi:[1,0]
	v_pk_mul_f32 v[12:13], v[12:13], v[18:19]
	v_cvt_pk_fp8_f32 v10, v14, v15 op_sel:[0,0,1]
	v_cvt_pk_fp8_f32 v11, v12, v13 op_sel:[0,0,1]
	s_nop 0
	v_permlane16_swap_b32_e32 v8, v10
	s_nop 0
	v_permlane16_swap_b32_e32 v9, v11
	global_store_dwordx4 v[0:1], v[8:11], off
	s_nop 1
	v_min_f32_e32 v9, v157, v6
	v_min_f32_e32 v8, v156, v6
	v_pk_mul_f32 v[10:11], v[8:9], s[84:85] op_sel_hi:[1,0]
	v_med3_f32 v13, v153, v7, v6
	v_exp_f32_e32 v10, v10
	v_exp_f32_e32 v11, v11
	v_med3_f32 v12, v152, v7, v6
	v_pk_add_f32 v[10:11], v[10:11], 1.0 op_sel_hi:[1,0]
	v_rcp_f32_e32 v10, v10
	v_rcp_f32_e32 v11, v11
	v_med3_f32 v15, v155, v7, v6
	v_med3_f32 v14, v154, v7, v6
	v_pk_mul_f32 v[8:9], v[8:9], v[10:11]
	v_pk_add_f32 v[10:11], v[12:13], 1.0 op_sel_hi:[1,0]
	v_pk_mul_f32 v[10:11], v[10:11], v[8:9]
	v_min_f32_e32 v9, v159, v6
	v_min_f32_e32 v8, v158, v6
; DI float kf(float c) { asm volatile("" : "+v"(c)); return c; }
; DI unsigned pk_fp8x4(float a, float b, float c, float d) { int p = 0; p = __builtin_amdgcn_cvt_pk_fp8_f32(a, b, p, false); p = __builtin_amdgcn_cvt_pk_fp8_f32(c, d, p, true); return (unsigned)p; }
;     DI void operator()(const f32x4 (&acc)[2][2][4][2], const Unit& u, int wr, int wc, int fr, int fq) const {
;         const int row0 = u.pm * BM + wr * 64 + fr + (fq & 1) * 16; const int col0 = u.pn * HALF + wc * 32 + 8 * (fq & ~1); const float c7 = kf(7.f);
; #pragma unroll
;         for (int ai = 0; ai < 2; ++ai)
; #pragma unroll
;             for (int mp = 0; mp < 2; ++mp) { unsigned char* rowp = O + (size_t)(row0 + ai * HALF + mp * 32) * ldc + col0;
;                 u32x2 w[2];
; #pragma unroll
;                 for (int mm = 0; mm < 2; ++mm) { const int m = 2 * mp + mm; float o[8];
; #pragma unroll
;                     for (int n = 0; n < 2; ++n) { const f32x4 g = acc[ai][0][m][n], l = acc[ai][1][m][n];
; #pragma unroll
;                         for (int jp = 0; jp < 2; ++jp) {
;                             const f32x2 xg = __builtin_elementwise_min((f32x2){g[2 * jp], g[2 * jp + 1]}, (f32x2){c7, c7});
;                             const f32x2 xl = __builtin_elementwise_min(__builtin_elementwise_max((f32x2){l[2 * jp], l[2 * jp + 1]}, (f32x2){-c7, -c7}), (f32x2){c7, c7});
;                             const f32x2 z = xg * (-1.702f * 1.44269504f); f32x2 e; e.x = __builtin_amdgcn_exp2f(z.x); e.y = __builtin_amdgcn_exp2f(z.y);
;                             const f32x2 dn = e + 1.f; f32x2 rc; rc.x = __builtin_amdgcn_rcpf(dn.x); rc.y = __builtin_amdgcn_rcpf(dn.y);
;                             const f32x2 r2 = (xg * rc) * (xl + 1.f); o[n * 4 + 2 * jp] = r2.x; o[n * 4 + 2 * jp + 1] = r2.y; } }
;                     w[mm].x = pk_fp8x4(o[0], o[1], o[2], o[3]); w[mm].y = pk_fp8x4(o[4], o[5], o[6], o[7]); }
;                 const u32x2 sx = __builtin_amdgcn_permlane16_swap(w[0].x, w[1].x, false, false), sy = __builtin_amdgcn_permlane16_swap(w[0].y, w[1].y, false, false);
;                 *(u32x4*)rowp = (u32x4){sx.x, sy.x, sx.y, sy.y}; }
	v_pk_mul_f32 v[12:13], v[8:9], s[84:85] op_sel_hi:[1,0]
	v_exp_f32_e32 v12, v12
	v_exp_f32_e32 v13, v13
	v_med3_f32 v17, v145, v7, v6
	v_med3_f32 v16, v144, v7, v6
	v_pk_add_f32 v[12:13], v[12:13], 1.0 op_sel_hi:[1,0]
	v_rcp_f32_e32 v12, v12
	v_rcp_f32_e32 v13, v13
	s_nop 0
	v_pk_mul_f32 v[8:9], v[8:9], v[12:13]
	v_pk_add_f32 v[12:13], v[14:15], 1.0 op_sel_hi:[1,0]
	v_med3_f32 v19, v147, v7, v6
	v_pk_mul_f32 v[12:13], v[12:13], v[8:9]
	v_min_f32_e32 v9, v149, v6
	v_min_f32_e32 v8, v148, v6
	v_pk_mul_f32 v[14:15], v[8:9], s[84:85] op_sel_hi:[1,0]
	v_med3_f32 v18, v146, v7, v6
	v_exp_f32_e32 v14, v14
	v_exp_f32_e32 v15, v15
	s_nop 0
	v_pk_add_f32 v[14:15], v[14:15], 1.0 op_sel_hi:[1,0]
	v_rcp_f32_e32 v14, v14
	v_rcp_f32_e32 v15, v15
	v_med3_f32 v21, v131, v7, v6
	v_med3_f32 v20, v130, v7, v6
	v_pk_mul_f32 v[8:9], v[8:9], v[14:15]
	v_pk_add_f32 v[14:15], v[16:17], 1.0 op_sel_hi:[1,0]
	s_nop 0
	v_pk_mul_f32 v[14:15], v[14:15], v[8:9]
	v_min_f32_e32 v9, v151, v6
	v_min_f32_e32 v8, v150, v6
	v_pk_mul_f32 v[16:17], v[8:9], s[84:85] op_sel_hi:[1,0]
	s_nop 0
	v_exp_f32_e32 v16, v16
	v_exp_f32_e32 v17, v17
	s_nop 0
	v_pk_add_f32 v[16:17], v[16:17], 1.0 op_sel_hi:[1,0]
	s_nop 0
	v_rcp_f32_e32 v16, v16
	v_rcp_f32_e32 v17, v17
	s_nop 0
	v_pk_mul_f32 v[16:17], v[8:9], v[16:17]
	v_mov_b32_e32 v9, v193
	v_cvt_pk_fp8_f32 v9, v14, v15
	v_mov_b32_e32 v8, v193
	v_cvt_pk_fp8_f32 v8, v10, v11
	v_pk_add_f32 v[10:11], v[18:19], 1.0 op_sel_hi:[1,0]
	v_pk_mul_f32 v[10:11], v[10:11], v[16:17]
	v_cvt_pk_fp8_f32 v8, v12, v13 op_sel:[0,0,1]
	v_cvt_pk_fp8_f32 v9, v10, v11 op_sel:[0,0,1]
	v_min_f32_e32 v11, v141, v6
	v_min_f32_e32 v10, v140, v6
	v_pk_mul_f32 v[12:13], v[10:11], s[84:85] op_sel_hi:[1,0]
	v_exp_f32_e32 v12, v12
	v_exp_f32_e32 v13, v13
	v_med3_f32 v15, v137, v7, v6
	v_pk_add_f32 v[12:13], v[12:13], 1.0 op_sel_hi:[1,0]
	v_med3_f32 v14, v136, v7, v6
	v_rcp_f32_e32 v12, v12
	v_rcp_f32_e32 v13, v13
	s_nop 0
	v_pk_mul_f32 v[10:11], v[10:11], v[12:13]
	v_pk_add_f32 v[12:13], v[14:15], 1.0 op_sel_hi:[1,0]
	v_pk_mul_f32 v[12:13], v[12:13], v[10:11]
	v_min_f32_e32 v11, v143, v6
	v_min_f32_e32 v10, v142, v6
	v_pk_mul_f32 v[14:15], v[10:11], s[84:85] op_sel_hi:[1,0]
	v_med3_f32 v17, v139, v7, v6
	v_exp_f32_e32 v14, v14
	v_exp_f32_e32 v15, v15
	v_med3_f32 v16, v138, v7, v6
	v_pk_add_f32 v[14:15], v[14:15], 1.0 op_sel_hi:[1,0]
	v_rcp_f32_e32 v14, v14
	v_rcp_f32_e32 v15, v15
	v_med3_f32 v19, v129, v7, v6
	v_med3_f32 v18, v128, v7, v6
	v_pk_mul_f32 v[10:11], v[10:11], v[14:15]
	v_pk_add_f32 v[14:15], v[16:17], 1.0 op_sel_hi:[1,0]
	s_nop 0
	v_pk_mul_f32 v[14:15], v[14:15], v[10:11]
	v_min_f32_e32 v11, v133, v6
	v_min_f32_e32 v10, v132, v6
	v_pk_mul_f32 v[16:17], v[10:11], s[84:85] op_sel_hi:[1,0]
	s_nop 0
	v_exp_f32_e32 v16, v16
	v_exp_f32_e32 v17, v17
	s_nop 0
	v_pk_add_f32 v[16:17], v[16:17], 1.0 op_sel_hi:[1,0]
	s_nop 0
	v_rcp_f32_e32 v16, v16
	v_rcp_f32_e32 v17, v17
	s_nop 0
	v_pk_mul_f32 v[10:11], v[10:11], v[16:17]
	v_pk_add_f32 v[16:17], v[18:19], 1.0 op_sel_hi:[1,0]
	s_nop 0
	v_pk_mul_f32 v[16:17], v[16:17], v[10:11]
	v_min_f32_e32 v11, v135, v6
	v_min_f32_e32 v10, v134, v6
	v_pk_mul_f32 v[18:19], v[10:11], s[84:85] op_sel_hi:[1,0]
	s_nop 0
	v_exp_f32_e32 v18, v18
	v_exp_f32_e32 v19, v19
	s_nop 0
	v_pk_add_f32 v[18:19], v[18:19], 1.0 op_sel_hi:[1,0]
	s_nop 0
	v_rcp_f32_e32 v18, v18
	v_rcp_f32_e32 v19, v19
	s_nop 0
	v_pk_mul_f32 v[18:19], v[10:11], v[18:19]
	v_mov_b32_e32 v10, v193
	v_mov_b32_e32 v11, v193
	v_cvt_pk_fp8_f32 v10, v12, v13
	v_cvt_pk_fp8_f32 v11, v16, v17
	v_pk_add_f32 v[12:13], v[20:21], 1.0 op_sel_hi:[1,0]
	v_pk_mul_f32 v[12:13], v[12:13], v[18:19]
	v_cvt_pk_fp8_f32 v10, v14, v15 op_sel:[0,0,1]
	v_cvt_pk_fp8_f32 v11, v12, v13 op_sel:[0,0,1]
	s_nop 0
	v_permlane16_swap_b32_e32 v8, v10
	s_nop 0
	v_permlane16_swap_b32_e32 v9, v11
	global_store_dwordx4 v[2:3], v[8:11], off
	v_min_f32_e32 v3, v125, v6
	v_min_f32_e32 v2, v124, v6
	v_pk_mul_f32 v[4:5], v[2:3], s[84:85] op_sel_hi:[1,0]
	v_exp_f32_e32 v4, v4
	v_exp_f32_e32 v5, v5
	s_nop 0
	v_pk_add_f32 v[4:5], v[4:5], 1.0 op_sel_hi:[1,0]
	v_med3_f32 v9, v121, v7, v6
	v_rcp_f32_e32 v4, v4
	v_rcp_f32_e32 v5, v5
	v_med3_f32 v8, v120, v7, v6
	v_pk_mul_f32 v[2:3], v[2:3], v[4:5]
	v_pk_add_f32 v[4:5], v[8:9], 1.0 op_sel_hi:[1,0]
	v_pk_mul_f32 v[4:5], v[4:5], v[2:3]
	v_min_f32_e32 v3, v127, v6
	v_min_f32_e32 v2, v126, v6
	v_pk_mul_f32 v[8:9], v[2:3], s[84:85] op_sel_hi:[1,0]
	v_exp_f32_e32 v8, v8
	v_exp_f32_e32 v9, v9
	v_med3_f32 v11, v123, v7, v6
	v_med3_f32 v10, v122, v7, v6
	v_pk_add_f32 v[8:9], v[8:9], 1.0 op_sel_hi:[1,0]
	v_rcp_f32_e32 v8, v8
	v_rcp_f32_e32 v9, v9
	v_med3_f32 v13, v113, v7, v6
	v_med3_f32 v12, v112, v7, v6
	v_pk_mul_f32 v[2:3], v[2:3], v[8:9]
	v_pk_add_f32 v[8:9], v[10:11], 1.0 op_sel_hi:[1,0]
	v_pk_mul_f32 v[8:9], v[8:9], v[2:3]
	v_min_f32_e32 v3, v117, v6
	v_min_f32_e32 v2, v116, v6
	v_pk_mul_f32 v[10:11], v[2:3], s[84:85] op_sel_hi:[1,0]
	v_exp_f32_e32 v10, v10
	v_exp_f32_e32 v11, v11
	v_med3_f32 v15, v115, v7, v6
	v_med3_f32 v14, v114, v7, v6
	v_pk_add_f32 v[10:11], v[10:11], 1.0 op_sel_hi:[1,0]
	v_rcp_f32_e32 v10, v10
	v_rcp_f32_e32 v11, v11
	v_med3_f32 v17, v99, v7, v6
	v_pk_mul_f32 v[2:3], v[2:3], v[10:11]
	v_pk_add_f32 v[10:11], v[12:13], 1.0 op_sel_hi:[1,0]
	v_med3_f32 v16, v98, v7, v6
	v_pk_mul_f32 v[10:11], v[10:11], v[2:3]
	v_min_f32_e32 v3, v119, v6
	v_min_f32_e32 v2, v118, v6
	v_pk_mul_f32 v[12:13], v[2:3], s[84:85] op_sel_hi:[1,0]
	s_nop 0
	v_exp_f32_e32 v12, v12
	v_exp_f32_e32 v13, v13
	s_nop 0
	v_pk_add_f32 v[12:13], v[12:13], 1.0 op_sel_hi:[1,0]
	s_nop 0
	v_rcp_f32_e32 v12, v12
	v_rcp_f32_e32 v13, v13
	s_nop 0
	v_pk_mul_f32 v[12:13], v[2:3], v[12:13]
	v_mov_b32_e32 v3, v193
; DI float kf(float c) { asm volatile("" : "+v"(c)); return c; }
; DI unsigned pk_fp8x4(float a, float b, float c, float d) { int p = 0; p = __builtin_amdgcn_cvt_pk_fp8_f32(a, b, p, false); p = __builtin_amdgcn_cvt_pk_fp8_f32(c, d, p, true); return (unsigned)p; }
;     DI void operator()(const f32x4 (&acc)[2][2][4][2], const Unit& u, int wr, int wc, int fr, int fq) const {
;         const int row0 = u.pm * BM + wr * 64 + fr + (fq & 1) * 16; const int col0 = u.pn * HALF + wc * 32 + 8 * (fq & ~1); const float c7 = kf(7.f);
; #pragma unroll
;         for (int ai = 0; ai < 2; ++ai)
; #pragma unroll
;             for (int mp = 0; mp < 2; ++mp) { unsigned char* rowp = O + (size_t)(row0 + ai * HALF + mp * 32) * ldc + col0;
;                 u32x2 w[2];
; #pragma unroll
;                 for (int mm = 0; mm < 2; ++mm) { const int m = 2 * mp + mm; float o[8];
; #pragma unroll
;                     for (int n = 0; n < 2; ++n) { const f32x4 g = acc[ai][0][m][n], l = acc[ai][1][m][n];
; #pragma unroll
;                         for (int jp = 0; jp < 2; ++jp) {
;                             const f32x2 xg = __builtin_elementwise_min((f32x2){g[2 * jp], g[2 * jp + 1]}, (f32x2){c7, c7});
;                             const f32x2 xl = __builtin_elementwise_min(__builtin_elementwise_max((f32x2){l[2 * jp], l[2 * jp + 1]}, (f32x2){-c7, -c7}), (f32x2){c7, c7});
;                             const f32x2 z = xg * (-1.702f * 1.44269504f); f32x2 e; e.x = __builtin_amdgcn_exp2f(z.x); e.y = __builtin_amdgcn_exp2f(z.y);
;                             const f32x2 dn = e + 1.f; f32x2 rc; rc.x = __builtin_amdgcn_rcpf(dn.x); rc.y = __builtin_amdgcn_rcpf(dn.y);
;                             const f32x2 r2 = (xg * rc) * (xl + 1.f); o[n * 4 + 2 * jp] = r2.x; o[n * 4 + 2 * jp + 1] = r2.y; } }
;                     w[mm].x = pk_fp8x4(o[0], o[1], o[2], o[3]); w[mm].y = pk_fp8x4(o[4], o[5], o[6], o[7]); }
;                 const u32x2 sx = __builtin_amdgcn_permlane16_swap(w[0].x, w[1].x, false, false), sy = __builtin_amdgcn_permlane16_swap(w[0].y, w[1].y, false, false);
;                 *(u32x4*)rowp = (u32x4){sx.x, sy.x, sx.y, sy.y}; }
	v_cvt_pk_fp8_f32 v3, v10, v11
	v_mov_b32_e32 v2, v193
	v_cvt_pk_fp8_f32 v2, v4, v5
	v_pk_add_f32 v[4:5], v[14:15], 1.0 op_sel_hi:[1,0]
	v_pk_mul_f32 v[4:5], v[4:5], v[12:13]
	v_cvt_pk_fp8_f32 v2, v8, v9 op_sel:[0,0,1]
	v_cvt_pk_fp8_f32 v3, v4, v5 op_sel:[0,0,1]
	v_min_f32_e32 v5, v109, v6
	v_min_f32_e32 v4, v108, v6
	v_pk_mul_f32 v[8:9], v[4:5], s[84:85] op_sel_hi:[1,0]
	v_exp_f32_e32 v8, v8
	v_exp_f32_e32 v9, v9
	v_med3_f32 v11, v105, v7, v6
	v_pk_add_f32 v[8:9], v[8:9], 1.0 op_sel_hi:[1,0]
	v_med3_f32 v10, v104, v7, v6
	v_rcp_f32_e32 v8, v8
	v_rcp_f32_e32 v9, v9
	s_nop 0
	v_pk_mul_f32 v[4:5], v[4:5], v[8:9]
	v_pk_add_f32 v[8:9], v[10:11], 1.0 op_sel_hi:[1,0]
	v_pk_mul_f32 v[8:9], v[8:9], v[4:5]
	v_min_f32_e32 v5, v111, v6
	v_min_f32_e32 v4, v110, v6
	v_pk_mul_f32 v[10:11], v[4:5], s[84:85] op_sel_hi:[1,0]
	v_med3_f32 v13, v107, v7, v6
	v_exp_f32_e32 v10, v10
	v_exp_f32_e32 v11, v11
	v_med3_f32 v12, v106, v7, v6
	v_pk_add_f32 v[10:11], v[10:11], 1.0 op_sel_hi:[1,0]
	v_rcp_f32_e32 v10, v10
	v_rcp_f32_e32 v11, v11
	v_med3_f32 v15, v97, v7, v6
	v_med3_f32 v14, v96, v7, v6
	v_pk_mul_f32 v[4:5], v[4:5], v[10:11]
	v_pk_add_f32 v[10:11], v[12:13], 1.0 op_sel_hi:[1,0]
	s_nop 0
	v_pk_mul_f32 v[10:11], v[10:11], v[4:5]
	v_min_f32_e32 v5, v101, v6
	v_min_f32_e32 v4, v100, v6
	v_pk_mul_f32 v[12:13], v[4:5], s[84:85] op_sel_hi:[1,0]
	s_nop 0
	v_exp_f32_e32 v12, v12
	v_exp_f32_e32 v13, v13
	s_nop 0
	v_pk_add_f32 v[12:13], v[12:13], 1.0 op_sel_hi:[1,0]
	s_nop 0
	v_rcp_f32_e32 v12, v12
	v_rcp_f32_e32 v13, v13
	s_nop 0
	v_pk_mul_f32 v[4:5], v[4:5], v[12:13]
	v_pk_add_f32 v[12:13], v[14:15], 1.0 op_sel_hi:[1,0]
	s_nop 0
	v_pk_mul_f32 v[12:13], v[12:13], v[4:5]
	v_min_f32_e32 v5, v103, v6
	v_min_f32_e32 v4, v102, v6
	v_pk_mul_f32 v[14:15], v[4:5], s[84:85] op_sel_hi:[1,0]
	s_nop 0
	v_exp_f32_e32 v14, v14
	v_exp_f32_e32 v15, v15
	s_nop 0
	v_pk_add_f32 v[14:15], v[14:15], 1.0 op_sel_hi:[1,0]
	s_nop 0
	v_rcp_f32_e32 v14, v14
	v_rcp_f32_e32 v15, v15
	s_nop 0
	v_pk_mul_f32 v[14:15], v[4:5], v[14:15]
	v_mov_b32_e32 v4, v193
	v_mov_b32_e32 v5, v193
	v_cvt_pk_fp8_f32 v4, v8, v9
	v_cvt_pk_fp8_f32 v5, v12, v13
	v_pk_add_f32 v[8:9], v[16:17], 1.0 op_sel_hi:[1,0]
	v_pk_mul_f32 v[8:9], v[8:9], v[14:15]
	v_cvt_pk_fp8_f32 v4, v10, v11 op_sel:[0,0,1]
	v_cvt_pk_fp8_f32 v5, v8, v9 op_sel:[0,0,1]
	v_add_co_u32_e32 v8, vcc, s2, v0
	v_permlane16_swap_b32_e32 v2, v4
	v_permlane16_swap_b32_e32 v3, v5
	v_addc_co_u32_e32 v9, vcc, 0, v1, vcc
	global_store_dwordx4 v[8:9], v[2:5], off
	s_nop 1
	v_min_f32_e32 v3, v93, v6
	v_min_f32_e32 v2, v92, v6
	v_pk_mul_f32 v[4:5], v[2:3], s[84:85] op_sel_hi:[1,0]
	v_exp_f32_e32 v4, v4
	v_exp_f32_e32 v5, v5
	v_med3_f32 v9, v89, v7, v6
	v_med3_f32 v8, v88, v7, v6
	v_pk_add_f32 v[4:5], v[4:5], 1.0 op_sel_hi:[1,0]
	v_rcp_f32_e32 v4, v4
	v_rcp_f32_e32 v5, v5
	s_nop 0
	v_pk_mul_f32 v[2:3], v[2:3], v[4:5]
	v_pk_add_f32 v[4:5], v[8:9], 1.0 op_sel_hi:[1,0]
	v_med3_f32 v11, v91, v7, v6
	v_pk_mul_f32 v[4:5], v[4:5], v[2:3]
	v_min_f32_e32 v3, v95, v6
	v_min_f32_e32 v2, v94, v6
	v_pk_mul_f32 v[8:9], v[2:3], s[84:85] op_sel_hi:[1,0]
	v_med3_f32 v10, v90, v7, v6
	v_exp_f32_e32 v8, v8
	v_exp_f32_e32 v9, v9
	s_nop 0
	v_pk_add_f32 v[8:9], v[8:9], 1.0 op_sel_hi:[1,0]
	v_med3_f32 v13, v81, v7, v6
	v_rcp_f32_e32 v8, v8
	v_rcp_f32_e32 v9, v9
	v_med3_f32 v12, v80, v7, v6
	v_pk_mul_f32 v[2:3], v[2:3], v[8:9]
	v_pk_add_f32 v[8:9], v[10:11], 1.0 op_sel_hi:[1,0]
	v_pk_mul_f32 v[8:9], v[8:9], v[2:3]
	v_min_f32_e32 v3, v85, v6
	v_min_f32_e32 v2, v84, v6
	v_pk_mul_f32 v[10:11], v[2:3], s[84:85] op_sel_hi:[1,0]
	v_exp_f32_e32 v10, v10
	v_exp_f32_e32 v11, v11
	v_med3_f32 v15, v83, v7, v6
	v_med3_f32 v14, v82, v7, v6
	v_pk_add_f32 v[10:11], v[10:11], 1.0 op_sel_hi:[1,0]
	v_rcp_f32_e32 v10, v10
	v_rcp_f32_e32 v11, v11
	v_max_f32_e32 v16, v66, v7
	v_add_co_u32_e32 v0, vcc, 0x28000, v0
	v_pk_mul_f32 v[2:3], v[2:3], v[10:11]
	v_pk_add_f32 v[10:11], v[12:13], 1.0 op_sel_hi:[1,0]
	v_addc_co_u32_e32 v1, vcc, 0, v1, vcc
	v_pk_mul_f32 v[10:11], v[10:11], v[2:3]
	v_min_f32_e32 v3, v87, v6
	v_min_f32_e32 v2, v86, v6
	v_pk_mul_f32 v[12:13], v[2:3], s[84:85] op_sel_hi:[1,0]
	s_andn2_b64 vcc, exec, s[36:37]
	v_exp_f32_e32 v12, v12
	v_exp_f32_e32 v13, v13
	s_nop 0
	v_pk_add_f32 v[12:13], v[12:13], 1.0 op_sel_hi:[1,0]
	s_nop 0
	v_rcp_f32_e32 v12, v12
	v_rcp_f32_e32 v13, v13
	s_nop 0
	v_pk_mul_f32 v[12:13], v[2:3], v[12:13]
	v_mov_b32_e32 v3, v193
	v_cvt_pk_fp8_f32 v3, v10, v11
	v_mov_b32_e32 v2, v193
	v_cvt_pk_fp8_f32 v2, v4, v5
	v_pk_add_f32 v[4:5], v[14:15], 1.0 op_sel_hi:[1,0]
	v_pk_mul_f32 v[4:5], v[4:5], v[12:13]
	v_cvt_pk_fp8_f32 v2, v8, v9 op_sel:[0,0,1]
	v_cvt_pk_fp8_f32 v3, v4, v5 op_sel:[0,0,1]
	v_min_f32_e32 v5, v77, v6
	v_min_f32_e32 v4, v76, v6
	v_pk_mul_f32 v[8:9], v[4:5], s[84:85] op_sel_hi:[1,0]
	v_exp_f32_e32 v8, v8
	v_exp_f32_e32 v9, v9
	v_med3_f32 v11, v73, v7, v6
	v_pk_add_f32 v[8:9], v[8:9], 1.0 op_sel_hi:[1,0]
	v_med3_f32 v10, v72, v7, v6
	v_rcp_f32_e32 v8, v8
	v_rcp_f32_e32 v9, v9
	s_nop 0
	v_pk_mul_f32 v[4:5], v[4:5], v[8:9]
	v_pk_add_f32 v[8:9], v[10:11], 1.0 op_sel_hi:[1,0]
	v_pk_mul_f32 v[8:9], v[8:9], v[4:5]
	v_min_f32_e32 v5, v79, v6
	v_min_f32_e32 v4, v78, v6
	v_pk_mul_f32 v[10:11], v[4:5], s[84:85] op_sel_hi:[1,0]
	v_med3_f32 v13, v75, v7, v6
	v_exp_f32_e32 v10, v10
	v_exp_f32_e32 v11, v11
	v_med3_f32 v12, v74, v7, v6
	v_pk_add_f32 v[10:11], v[10:11], 1.0 op_sel_hi:[1,0]
	v_rcp_f32_e32 v10, v10
	v_rcp_f32_e32 v11, v11
	v_med3_f32 v15, v65, v7, v6
	v_med3_f32 v14, v64, v7, v6
	v_pk_mul_f32 v[4:5], v[4:5], v[10:11]
	v_pk_add_f32 v[10:11], v[12:13], 1.0 op_sel_hi:[1,0]
	v_max_f32_e32 v7, v67, v7
	v_pk_mul_f32 v[10:11], v[10:11], v[4:5]
	v_min_f32_e32 v5, v69, v6
	v_min_f32_e32 v4, v68, v6
	v_pk_mul_f32 v[12:13], v[4:5], s[84:85] op_sel_hi:[1,0]
	v_min_f32_e32 v7, v7, v6
	v_exp_f32_e32 v12, v12
	v_exp_f32_e32 v13, v13
	s_nop 0
	v_pk_add_f32 v[12:13], v[12:13], 1.0 op_sel_hi:[1,0]
	s_nop 0
	v_rcp_f32_e32 v12, v12
	v_rcp_f32_e32 v13, v13
	s_nop 0
	v_pk_mul_f32 v[4:5], v[4:5], v[12:13]
	v_pk_add_f32 v[12:13], v[14:15], 1.0 op_sel_hi:[1,0]
	s_nop 0
	v_pk_mul_f32 v[12:13], v[12:13], v[4:5]
	v_min_f32_e32 v5, v71, v6
	v_min_f32_e32 v4, v70, v6
	v_pk_mul_f32 v[14:15], v[4:5], s[84:85] op_sel_hi:[1,0]
	v_min_f32_e32 v6, v16, v6
	v_exp_f32_e32 v14, v14
	v_exp_f32_e32 v15, v15
	v_pk_add_f32 v[6:7], v[6:7], 1.0 op_sel_hi:[1,0]
	v_pk_add_f32 v[14:15], v[14:15], 1.0 op_sel_hi:[1,0]
	s_nop 0
	v_rcp_f32_e32 v14, v14
	v_rcp_f32_e32 v15, v15
	s_nop 0
	v_pk_mul_f32 v[14:15], v[4:5], v[14:15]
	v_mov_b32_e32 v4, v193
	v_mov_b32_e32 v5, v193
	v_cvt_pk_fp8_f32 v4, v8, v9
	v_cvt_pk_fp8_f32 v5, v12, v13
	v_pk_mul_f32 v[6:7], v[6:7], v[14:15]
	v_cvt_pk_fp8_f32 v4, v10, v11 op_sel:[0,0,1]
	v_cvt_pk_fp8_f32 v5, v6, v7 op_sel:[0,0,1]
	s_nop 0
	v_permlane16_swap_b32_e32 v2, v4
	v_permlane16_swap_b32_e32 v3, v5
	global_store_dwordx4 v[0:1], v[2:5], off
	s_cbranch_vccnz .LBB0_1178
	v_add_u32_e32 v0, s6, v232
	ds_read_b128 v[76:79], v0 offset:1024
	ds_read_b128 v[68:71], v0 offset:1040
	ds_read_b128 v[72:75], v0 offset:1536
	ds_read_b128 v[64:67], v0 offset:1552
	s_andn2_b64 vcc, exec, s[44:45]
	s_cbranch_vccnz .LBB0_1177
	s_barrier
	s_branch .LBB0_1177
